# speedup vs baseline: 1.0041x; 1.0041x over previous
.LBB0_17:
	s_lshl_b32 s14, s18, 4
	s_lshl_b32 s15, s18, 6
	s_or_b32 s21, s14, 1
	v_or_b32_e32 v48, s15, v31
	v_readlane_b32 s22, v2, s14
	v_or_b32_e32 v49, s15, v32
	v_readlane_b32 s31, v2, s21
	ds_bpermute_b32 v64, v48, v4
	v_or_b32_e32 v50, s15, v33
	v_or_b32_e32 v60, s15, v34
	v_or_b32_e32 v61, s15, v35
	ds_bpermute_b32 v65, v48, v5
	ds_bpermute_b32 v66, v49, v4
	ds_bpermute_b32 v67, v49, v5
	v_mov_b32_e32 v70, s22
	s_waitcnt vmcnt(3)
	v_fma_f32 v85, v70, v54, v58
	s_waitcnt vmcnt(0)
	v_fma_f32 v86, -v70, v3, v55
	v_mov_b32_e32 v87, s31
	v_fma_f32 v3, v70, v55, v3
	v_fma_f32 v54, -v70, v58, v54
	v_fma_f32 v91, v87, v53, v56
	v_fma_f32 v53, -v87, v56, v53
	ds_bpermute_b32 v56, v20, v54
	s_waitcnt lgkmcnt(2)
	v_mul_f32 v98, v64, v66
	s_waitcnt lgkmcnt(1)
	v_mul_f32 v64, v64, v67
	v_or_b32_e32 v51, s15, v21
	v_bitop3_b32 v59, s15, 36, v21 bitop3:0x36
	ds_bpermute_b32 v48, v48, v2
	ds_bpermute_b32 v68, v50, v4
	ds_bpermute_b32 v69, v50, v5
	ds_bpermute_b32 v77, v60, v4
	ds_bpermute_b32 v78, v60, v5
	ds_bpermute_b32 v79, v61, v4
	ds_bpermute_b32 v80, v61, v5
	v_fma_f32 v92, -v87, v57, v52
	v_fma_f32 v52, v87, v52, v57
	ds_bpermute_b32 v57, v20, v3
	s_waitcnt lgkmcnt(2)
	v_mul_f32 v99, v77, v79
	v_fma_f32 v67, -v65, v67, v98
	v_fma_f32 v64, v65, v66, v64
	v_fma_f32 v3, v48, v56, v3
	v_or_b32_e32 v62, s15, v22
	s_waitcnt lgkmcnt(1)
	v_fma_f32 v65, -v78, v80, v99
	v_mul_f32 v56, v67, v68
	ds_bpermute_b32 v49, v49, v2
	ds_bpermute_b32 v73, v51, v4 offset:32
	ds_bpermute_b32 v74, v51, v5 offset:32
	ds_bpermute_b32 v75, v59, v4
	ds_bpermute_b32 v76, v59, v5
	ds_bpermute_b32 v94, v20, v53
	ds_bpermute_b32 v95, v20, v52
	v_mul_f32 v77, v77, v80
	s_waitcnt lgkmcnt(7)
	v_fma_f32 v54, -v48, v57, v54
	v_mul_f32 v57, v67, v69
	s_waitcnt lgkmcnt(5)
	v_mul_f32 v67, v65, v73
	s_waitcnt lgkmcnt(3)
	v_mul_f32 v80, v65, v75
	s_waitcnt lgkmcnt(1)
	v_fma_f32 v52, v48, v94, v52
	v_fma_f32 v66, v78, v79, v77
	v_mul_f32 v79, v65, v74
	v_mul_f32 v65, v65, v76
	v_fma_f32 v56, -v64, v69, v56
	v_mov_b32_dpp v69, v52 row_mirror row_mask:0xf bank_mask:0xf bound_ctrl:1
	s_nop 1
	v_mov_b32_dpp v69, v69 quad_perm:[3,2,1,0] row_mask:0xf bank_mask:0xf bound_ctrl:1
	ds_bpermute_b32 v81, v62, v4 offset:56
	ds_bpermute_b32 v82, v62, v5 offset:56
	ds_bpermute_b32 v87, v20, v86
	ds_bpermute_b32 v93, v20, v85
	ds_bpermute_b32 v96, v20, v92
	ds_bpermute_b32 v97, v20, v91
	s_waitcnt lgkmcnt(3)
	v_fma_f32 v77, v48, v87, v85
	s_waitcnt lgkmcnt(2)
	v_fma_f32 v78, -v48, v93, v86
	s_waitcnt lgkmcnt(1)
	v_fma_f32 v85, v48, v96, v91
	s_waitcnt lgkmcnt(0)
	v_fma_f32 v86, -v48, v97, v92
	v_fma_f32 v48, -v48, v95, v53
	v_fma_f32 v57, v64, v68, v57
	v_fma_f32 v64, -v66, v74, v67
	v_fma_f32 v67, v66, v73, v79
	v_fma_f32 v68, -v66, v76, v80
	v_fma_f32 v65, v66, v75, v65
	v_mov_b32_dpp v66, v48 row_mirror row_mask:0xf bank_mask:0xf bound_ctrl:1
	v_mov_b32_dpp v74, v85 row_mirror row_mask:0xf bank_mask:0xf bound_ctrl:1
	s_nop 0
	v_mov_b32_dpp v66, v66 quad_perm:[3,2,1,0] row_mask:0xf bank_mask:0xf bound_ctrl:1
	v_mov_b32_dpp v74, v74 quad_perm:[3,2,1,0] row_mask:0xf bank_mask:0xf bound_ctrl:1
	v_readlane_b32 s19, v4, s14
	v_readlane_b32 s20, v5, s14
	v_bitop3_b32 v63, s15, 60, v22 bitop3:0x36
	v_readlane_b32 s29, v4, s21
	v_readlane_b32 s30, v5, s21
	v_mov_b32_e32 v71, s19
	v_mov_b32_e32 v72, s20
	ds_bpermute_b32 v83, v63, v4
	ds_bpermute_b32 v84, v63, v5
	v_mov_b32_e32 v55, s29
	v_mov_b32_e32 v58, s30
	v_mov_b32_dpp v53, v54 row_mirror row_mask:0xf bank_mask:0xf bound_ctrl:1
	v_mov_b32_dpp v73, v86 row_mirror row_mask:0xf bank_mask:0xf bound_ctrl:1
	s_nop 0
	v_mov_b32_dpp v53, v53 quad_perm:[3,2,1,0] row_mask:0xf bank_mask:0xf bound_ctrl:1
	v_mov_b32_dpp v73, v73 quad_perm:[3,2,1,0] row_mask:0xf bank_mask:0xf bound_ctrl:1
	v_mul_f32 v75, v56, v71
	v_mul_f32 v76, v56, v72
	v_mul_f32 v79, v56, v55
	v_mul_f32 v56, v56, v58
	v_mul_f32 v80, v64, v81
	v_mul_f32 v93, v64, v82
	s_waitcnt lgkmcnt(1)
	v_mul_f32 v94, v64, v83
	s_waitcnt lgkmcnt(0)
	v_mul_f32 v64, v64, v84
	v_mul_f32 v95, v68, v81
	v_mul_f32 v96, v68, v82
	v_mul_f32 v97, v68, v83
	v_mul_f32 v68, v68, v84
	ds_bpermute_b32 v50, v50, v2
	v_mov_b32_dpp v87, v3 row_mirror row_mask:0xf bank_mask:0xf bound_ctrl:1
	v_mov_b32_dpp v91, v78 row_mirror row_mask:0xf bank_mask:0xf bound_ctrl:1
	v_mov_b32_dpp v92, v77 row_mirror row_mask:0xf bank_mask:0xf bound_ctrl:1
	v_mov_b32_dpp v87, v87 quad_perm:[3,2,1,0] row_mask:0xf bank_mask:0xf bound_ctrl:1
	v_mov_b32_dpp v91, v91 quad_perm:[3,2,1,0] row_mask:0xf bank_mask:0xf bound_ctrl:1
	v_mov_b32_dpp v92, v92 quad_perm:[3,2,1,0] row_mask:0xf bank_mask:0xf bound_ctrl:1
	v_fma_f32 v72, -v57, v72, v75
	v_fma_f32 v71, v57, v71, v76
	v_fma_f32 v58, -v57, v58, v79
	v_fma_f32 v55, v57, v55, v56
	v_fma_f32 v56, -v67, v82, v80
	v_fma_f32 v57, v67, v81, v93
	v_fma_f32 v75, -v67, v84, v94
	v_fma_f32 v64, v67, v83, v64
	v_fma_f32 v67, -v65, v82, v95
	v_fma_f32 v76, v65, v81, v96
	v_fma_f32 v79, -v65, v84, v97
	v_fma_f32 v65, v65, v83, v68
	s_waitcnt lgkmcnt(0)
	v_fma_f32 v68, v49, v91, v77
	s_waitcnt lgkmcnt(0)
	v_fma_f32 v77, -v49, v92, v78
	v_fma_f32 v3, v49, v53, v3
	v_fma_f32 v53, -v49, v87, v54
	v_fma_f32 v54, v49, v73, v85
	v_fma_f32 v73, -v49, v74, v86
	v_fma_f32 v52, v49, v66, v52
	v_fma_f32 v48, -v49, v69, v48
	v_mov_b32_dpp v69, v77 quad_perm:[3,2,1,0] row_mask:0xf bank_mask:0xf bound_ctrl:1
	v_mov_b32_dpp v49, v53 quad_perm:[3,2,1,0] row_mask:0xf bank_mask:0xf bound_ctrl:1
	v_mov_b32_dpp v66, v3 quad_perm:[3,2,1,0] row_mask:0xf bank_mask:0xf bound_ctrl:1
	v_mov_b32_dpp v74, v68 quad_perm:[3,2,1,0] row_mask:0xf bank_mask:0xf bound_ctrl:1
	v_mov_b32_dpp v78, v48 quad_perm:[3,2,1,0] row_mask:0xf bank_mask:0xf bound_ctrl:1
	v_mov_b32_dpp v80, v52 quad_perm:[3,2,1,0] row_mask:0xf bank_mask:0xf bound_ctrl:1
	v_mov_b32_dpp v81, v73 quad_perm:[3,2,1,0] row_mask:0xf bank_mask:0xf bound_ctrl:1
	v_mov_b32_dpp v82, v54 quad_perm:[3,2,1,0] row_mask:0xf bank_mask:0xf bound_ctrl:1
	v_fma_f32 v68, v50, v69, v68
	v_fma_f32 v69, -v50, v74, v77
	v_fma_f32 v3, v50, v49, v3
	v_fma_f32 v49, -v50, v66, v53
	v_fma_f32 v53, v50, v81, v54
	v_fma_f32 v54, -v50, v82, v73
	v_fma_f32 v52, v50, v78, v52
	v_fma_f32 v48, -v50, v80, v48
	v_mul_f32 v66, v72, v3
	v_mul_f32 v50, v72, v49
	ds_bpermute_b32 v51, v51, v2 offset:32
	v_fma_f32 v3, -v71, v3, v50
	v_mul_f32 v50, v58, v48
	v_mul_f32 v73, v72, v69
	v_mul_f32 v72, v72, v68
	v_fma_f32 v49, v71, v49, v66
	v_mul_f32 v66, v58, v52
	v_mul_f32 v74, v58, v54
	v_mul_f32 v58, v58, v53
	s_nop 0
	v_fma_f32 v50, -v55, v52, v50
	ds_bpermute_b32 v59, v59, v2
	v_fma_f32 v48, v55, v48, v66
	v_fma_f32 v52, -v55, v53, v74
	v_fma_f32 v53, v55, v54, v58
	ds_bpermute_b32 v54, v19, v3
	ds_bpermute_b32 v55, v19, v49
	v_fma_f32 v68, -v71, v68, v73
	v_fma_f32 v69, v71, v69, v72
	ds_bpermute_b32 v58, v19, v68
	ds_bpermute_b32 v66, v19, v69
	ds_bpermute_b32 v71, v19, v50
	ds_bpermute_b32 v72, v19, v48
	ds_bpermute_b32 v73, v19, v52
	ds_bpermute_b32 v74, v19, v53
	s_waitcnt lgkmcnt(5)
	v_fma_f32 v53, v51, v58, v53
	s_waitcnt lgkmcnt(4)
	v_fma_f32 v52, -v51, v66, v52
	v_fma_f32 v48, v59, v54, v48
	v_fma_f32 v50, -v59, v55, v50
	s_waitcnt lgkmcnt(1)
	v_fma_f32 v54, v59, v73, v69
	s_waitcnt lgkmcnt(0)
	v_fma_f32 v55, -v59, v74, v68
	v_fma_f32 v49, v51, v71, v49
	v_fma_f32 v3, -v51, v72, v3
	ds_swizzle_b32 v51, v50 offset:swizzle(BITMASK_PERM,"iippp")
	ds_bpermute_b32 v60, v60, v2
	ds_swizzle_b32 v58, v48 offset:swizzle(BITMASK_PERM,"iippp")
	ds_swizzle_b32 v59, v52 offset:swizzle(BITMASK_PERM,"iippp")
	ds_swizzle_b32 v66, v53 offset:swizzle(BITMASK_PERM,"iippp")
	ds_swizzle_b32 v68, v3 offset:swizzle(BITMASK_PERM,"iippp")
	ds_swizzle_b32 v69, v49 offset:swizzle(BITMASK_PERM,"iippp")
	ds_swizzle_b32 v71, v55 offset:swizzle(BITMASK_PERM,"iippp")
	ds_swizzle_b32 v72, v54 offset:swizzle(BITMASK_PERM,"iippp")
	s_waitcnt lgkmcnt(7)
	v_fma_f32 v48, v60, v51, v48
	s_waitcnt lgkmcnt(6)
	v_fma_f32 v50, -v60, v58, v50
	s_waitcnt lgkmcnt(1)
	v_fma_f32 v51, v60, v71, v54
	s_waitcnt lgkmcnt(0)
	v_fma_f32 v54, -v60, v72, v55
	v_mov_b32_dpp v55, v50 row_half_mirror row_mask:0xf bank_mask:0xf bound_ctrl:1
	s_nop 1
	v_mov_b32_dpp v55, v55 quad_perm:[1,0,3,2] row_mask:0xf bank_mask:0xf bound_ctrl:1
	ds_bpermute_b32 v61, v61, v2
	v_fma_f32 v53, v60, v59, v53
	v_fma_f32 v52, -v60, v66, v52
	v_fma_f32 v49, v60, v68, v49
	v_fma_f32 v3, -v60, v69, v3
	v_mov_b32_dpp v58, v48 row_half_mirror row_mask:0xf bank_mask:0xf bound_ctrl:1
	v_mov_b32_dpp v59, v52 row_half_mirror row_mask:0xf bank_mask:0xf bound_ctrl:1
	v_mov_b32_dpp v60, v53 row_half_mirror row_mask:0xf bank_mask:0xf bound_ctrl:1
	v_mov_b32_dpp v66, v3 row_half_mirror row_mask:0xf bank_mask:0xf bound_ctrl:1
	v_mov_b32_dpp v68, v49 row_half_mirror row_mask:0xf bank_mask:0xf bound_ctrl:1
	v_mov_b32_dpp v69, v54 row_half_mirror row_mask:0xf bank_mask:0xf bound_ctrl:1
	v_mov_b32_dpp v58, v58 quad_perm:[1,0,3,2] row_mask:0xf bank_mask:0xf bound_ctrl:1
	v_mov_b32_dpp v59, v59 quad_perm:[1,0,3,2] row_mask:0xf bank_mask:0xf bound_ctrl:1
	v_mov_b32_dpp v60, v60 quad_perm:[1,0,3,2] row_mask:0xf bank_mask:0xf bound_ctrl:1
	v_mov_b32_dpp v66, v66 quad_perm:[1,0,3,2] row_mask:0xf bank_mask:0xf bound_ctrl:1
	v_mov_b32_dpp v68, v68 quad_perm:[1,0,3,2] row_mask:0xf bank_mask:0xf bound_ctrl:1
	v_mov_b32_dpp v69, v69 quad_perm:[1,0,3,2] row_mask:0xf bank_mask:0xf bound_ctrl:1
	ds_bpermute_b32 v62, v62, v2 offset:56
	v_mov_b32_dpp v71, v51 row_half_mirror row_mask:0xf bank_mask:0xf bound_ctrl:1
	s_nop 1
	v_mov_b32_dpp v71, v71 quad_perm:[1,0,3,2] row_mask:0xf bank_mask:0xf bound_ctrl:1
	s_waitcnt lgkmcnt(1)
	v_fma_f32 v53, v61, v59, v53
	s_waitcnt lgkmcnt(1)
	v_fma_f32 v52, -v61, v60, v52
	v_fma_f32 v48, v61, v55, v48
	v_fma_f32 v50, -v61, v58, v50
	s_waitcnt lgkmcnt(1)
	v_fma_f32 v51, v61, v69, v51
	s_waitcnt lgkmcnt(0)
	v_fma_f32 v54, -v61, v71, v54
	v_fma_f32 v49, v61, v66, v49
	v_fma_f32 v3, -v61, v68, v3
	v_mov_b32_dpp v55, v52 quad_perm:[1,0,3,2] row_mask:0xf bank_mask:0xf bound_ctrl:1
	ds_bpermute_b32 v63, v63, v2
	v_mov_b32_dpp v58, v53 quad_perm:[1,0,3,2] row_mask:0xf bank_mask:0xf bound_ctrl:1
	v_mov_b32_dpp v59, v50 quad_perm:[1,0,3,2] row_mask:0xf bank_mask:0xf bound_ctrl:1
	v_mov_b32_dpp v60, v48 quad_perm:[1,0,3,2] row_mask:0xf bank_mask:0xf bound_ctrl:1
	v_mov_b32_dpp v61, v54 quad_perm:[1,0,3,2] row_mask:0xf bank_mask:0xf bound_ctrl:1
	v_mov_b32_dpp v66, v51 quad_perm:[1,0,3,2] row_mask:0xf bank_mask:0xf bound_ctrl:1
	v_mov_b32_dpp v68, v3 quad_perm:[1,0,3,2] row_mask:0xf bank_mask:0xf bound_ctrl:1
	v_mov_b32_dpp v69, v49 quad_perm:[1,0,3,2] row_mask:0xf bank_mask:0xf bound_ctrl:1
	s_waitcnt lgkmcnt(0)
	v_fma_f32 v51, v63, v59, v51
	v_fma_f32 v54, -v63, v60, v54
	v_fma_f32 v49, v62, v55, v49
	v_fma_f32 v3, -v62, v58, v3
	v_fma_f32 v53, v63, v68, v53
	v_fma_f32 v52, -v63, v69, v52
	v_fma_f32 v48, v62, v61, v48
	v_fma_f32 v50, -v62, v66, v50
	v_mul_f32 v58, v79, v54
	v_mul_f32 v55, v56, v3
	v_mul_f32 v56, v56, v49
	v_mul_f32 v59, v79, v51
	v_mul_f32 v60, v75, v53
	s_or_b32 s23, s14, 3
	v_fma_f32 v49, -v57, v49, v55
	v_fma_f32 v3, v57, v3, v56
	v_mul_f32 v55, v67, v50
	v_mul_f32 v56, v67, v48
	v_mul_f32 v57, v75, v52
	v_fma_f32 v51, -v65, v51, v58
	v_fma_f32 v54, v65, v54, v59
	v_fma_f32 v52, v64, v52, v60
	v_fma_f32 v48, -v76, v48, v55
	v_fma_f32 v50, v76, v50, v56
	v_fma_f32 v53, -v64, v53, v57
	s_or_b32 s24, s14, 2
	v_fmac_f32_dpp v49, v49, v23 quad_perm:[1,0,3,2] row_mask:0xf bank_mask:0xf
	v_fmac_f32_dpp v48, v48, v23 quad_perm:[1,0,3,2] row_mask:0xf bank_mask:0xf
	v_fmac_f32_dpp v53, v53, v23 quad_perm:[1,0,3,2] row_mask:0xf bank_mask:0xf
	v_fmac_f32_dpp v51, v51, v23 quad_perm:[1,0,3,2] row_mask:0xf bank_mask:0xf
	v_fmac_f32_dpp v3, v3, v23 quad_perm:[1,0,3,2] row_mask:0xf bank_mask:0xf
	v_fmac_f32_dpp v50, v50, v23 quad_perm:[1,0,3,2] row_mask:0xf bank_mask:0xf
	v_fmac_f32_dpp v52, v52, v23 quad_perm:[1,0,3,2] row_mask:0xf bank_mask:0xf
	v_fmac_f32_dpp v54, v54, v23 quad_perm:[1,0,3,2] row_mask:0xf bank_mask:0xf

	v_readlane_b32 s20, v45, s23
	s_nop 1
	v_fmac_f32_dpp v49, v49, v24 quad_perm:[2,3,0,1] row_mask:0xf bank_mask:0xf
	v_fmac_f32_dpp v48, v48, v24 quad_perm:[2,3,0,1] row_mask:0xf bank_mask:0xf
	v_fmac_f32_dpp v53, v53, v24 quad_perm:[2,3,0,1] row_mask:0xf bank_mask:0xf
	v_fmac_f32_dpp v51, v51, v24 quad_perm:[2,3,0,1] row_mask:0xf bank_mask:0xf
	v_fmac_f32_dpp v3, v3, v24 quad_perm:[2,3,0,1] row_mask:0xf bank_mask:0xf
	v_fmac_f32_dpp v50, v50, v24 quad_perm:[2,3,0,1] row_mask:0xf bank_mask:0xf
	v_fmac_f32_dpp v52, v52, v24 quad_perm:[2,3,0,1] row_mask:0xf bank_mask:0xf
	v_fmac_f32_dpp v54, v54, v24 quad_perm:[2,3,0,1] row_mask:0xf bank_mask:0xf

	v_readlane_b32 s19, v45, s24
	v_readlane_b32 s15, v45, s14
	v_mov_b32_dpp v55, v49 row_half_mirror row_mask:0xf bank_mask:0xf bound_ctrl:1
	v_mov_b32_dpp v56, v48 row_half_mirror row_mask:0xf bank_mask:0xf bound_ctrl:1
	v_mov_b32_dpp v57, v53 row_half_mirror row_mask:0xf bank_mask:0xf bound_ctrl:1
	v_mov_b32_dpp v58, v51 row_half_mirror row_mask:0xf bank_mask:0xf bound_ctrl:1
	v_mov_b32_dpp v59, v3 row_half_mirror row_mask:0xf bank_mask:0xf bound_ctrl:1
	v_mov_b32_dpp v60, v50 row_half_mirror row_mask:0xf bank_mask:0xf bound_ctrl:1
	v_mov_b32_dpp v61, v52 row_half_mirror row_mask:0xf bank_mask:0xf bound_ctrl:1
	v_mov_b32_dpp v62, v54 row_half_mirror row_mask:0xf bank_mask:0xf bound_ctrl:1
	v_fmac_f32_dpp v49, v55, v25 quad_perm:[3,2,1,0] row_mask:0xf bank_mask:0xf
	v_fmac_f32_dpp v48, v56, v25 quad_perm:[3,2,1,0] row_mask:0xf bank_mask:0xf
	v_fmac_f32_dpp v53, v57, v25 quad_perm:[3,2,1,0] row_mask:0xf bank_mask:0xf
	v_fmac_f32_dpp v51, v58, v25 quad_perm:[3,2,1,0] row_mask:0xf bank_mask:0xf
	v_fmac_f32_dpp v3, v59, v25 quad_perm:[3,2,1,0] row_mask:0xf bank_mask:0xf
	v_fmac_f32_dpp v50, v60, v25 quad_perm:[3,2,1,0] row_mask:0xf bank_mask:0xf
	v_fmac_f32_dpp v52, v61, v25 quad_perm:[3,2,1,0] row_mask:0xf bank_mask:0xf
	v_fmac_f32_dpp v54, v62, v25 quad_perm:[3,2,1,0] row_mask:0xf bank_mask:0xf

	s_or_b32 s25, s14, 4
	v_fmac_f32_dpp v49, v49, v26 row_ror:8 row_mask:0xf bank_mask:0xf
	v_fmac_f32_dpp v48, v48, v26 row_ror:8 row_mask:0xf bank_mask:0xf
	v_fmac_f32_dpp v53, v53, v26 row_ror:8 row_mask:0xf bank_mask:0xf
	v_fmac_f32_dpp v51, v51, v26 row_ror:8 row_mask:0xf bank_mask:0xf
	v_fmac_f32_dpp v3, v3, v26 row_ror:8 row_mask:0xf bank_mask:0xf
	v_fmac_f32_dpp v50, v50, v26 row_ror:8 row_mask:0xf bank_mask:0xf
	v_fmac_f32_dpp v52, v52, v26 row_ror:8 row_mask:0xf bank_mask:0xf
	v_fmac_f32_dpp v54, v54, v26 row_ror:8 row_mask:0xf bank_mask:0xf

	s_or_b32 s26, s14, 5
	v_add_f32 v55, v49, v48
	v_sub_f32 v48, v49, v48
	v_add_f32 v49, v3, v50
	v_sub_f32 v3, v3, v50
	v_add_f32 v50, v53, v51
	v_sub_f32 v51, v53, v51
	v_add_f32 v53, v52, v54
	v_sub_f32 v52, v52, v54
	s_or_b32 s27, s14, 6
	v_add_f32 v54, v55, v50
	v_sub_f32 v50, v55, v50
	v_add_f32 v55, v49, v53
	v_sub_f32 v49, v49, v53
	v_add_f32 v53, v48, v51
	v_sub_f32 v48, v48, v51
	v_add_f32 v51, v3, v52
	v_sub_f32 v3, v3, v52
	s_or_b32 s28, s14, 7
	v_permlane16_swap_b32 v54, v53
	v_permlane16_swap_b32 v55, v51
	v_permlane16_swap_b32 v50, v48
	v_permlane16_swap_b32 v49, v3
	v_readlane_b32 s14, v45, s21
	s_nop 1
	v_permlane32_swap_b32 v54, v50
	v_permlane32_swap_b32 v55, v49
	v_permlane32_swap_b32 v53, v48
	v_permlane32_swap_b32 v51, v3
	v_readlane_b32 s21, v45, s25
	v_add_f32 v52, v54, v53
	v_sub_f32 v53, v54, v53
	v_add_f32 v54, v55, v51
	v_sub_f32 v51, v55, v51
	v_add_f32 v55, v50, v48
	v_sub_f32 v48, v50, v48
	v_add_f32 v50, v49, v3
	v_sub_f32 v3, v49, v3
	v_readlane_b32 s22, v45, s26
	v_add_f32 v49, v52, v55
	v_sub_f32 v52, v52, v55
	v_add_f32 v55, v54, v50
	v_sub_f32 v50, v54, v50
	v_add_f32 v54, v53, v48
	v_sub_f32 v48, v53, v48
	v_add_f32 v53, v51, v3
	v_sub_f32 v3, v51, v3
	v_mul_f32 v49, v49, v7
	v_mul_f32 v51, v55, v7
	v_mul_f32 v54, v54, v8
	v_mul_f32 v48, v48, v10
	v_mul_f32 v53, v53, v8
	v_mul_f32 v3, v3, v10
	v_mul_f32 v52, v52, v9
	v_mul_f32 v50, v50, v9
	s_nop 0
	v_fma_f32 v56, -s20, v54, v51
	v_fma_f32 v51, s20, v51, v54
	v_fma_f32 v55, s20, v53, v49
	v_fma_f32 v49, -s20, v49, v53
	v_fma_f32 v53, s20, v3, v52
	v_fma_f32 v54, -s20, v48, v50
	v_fma_f32 v48, s20, v50, v48
	v_fma_f32 v3, -s20, v52, v3
	v_mov_b32_e32 v70, s21
	v_fma_f32 v50, s19, v54, v55
	v_fma_f32 v52, -s19, v53, v56
	v_fma_f32 v53, s19, v56, v53
	v_fma_f32 v54, -s19, v55, v54
	v_fma_f32 v55, s19, v3, v51
	v_fma_f32 v56, -s19, v48, v49
	v_fma_f32 v48, s19, v49, v48
	v_fma_f32 v3, -s19, v51, v3
	v_readlane_b32 s23, v45, s27
	s_nop 1
	v_permlane32_swap_b32 v50, v53
	v_permlane32_swap_b32 v52, v54
	v_permlane32_swap_b32 v55, v48
	v_permlane32_swap_b32 v56, v3
	v_mov_b32_e32 v88, s22
	s_nop 1
	v_permlane16_swap_b32 v50, v55
	v_permlane16_swap_b32 v52, v56
	v_permlane16_swap_b32 v53, v48
	v_permlane16_swap_b32 v54, v3
	s_and_b64 vcc, exec, s[10:11]
	v_fma_f32 v51, -s14, v55, v52
	v_fma_f32 v58, s14, v52, v55
	v_fma_f32 v52, s14, v3, v53
	v_fma_f32 v55, -s14, v48, v54
	v_fma_f32 v49, s14, v56, v50
	v_fma_f32 v50, -s14, v50, v56
	v_fma_f32 v48, s14, v54, v48
	v_fma_f32 v59, -s14, v53, v3
	s_nop 0
	v_fma_f32 v3, -s15, v52, v51
	v_fma_f32 v52, s15, v51, v52
	v_fma_f32 v54, s15, v55, v49
	v_fma_f32 v56, -s15, v49, v55
	v_fma_f32 v57, -s15, v48, v50
	v_fma_f32 v53, s15, v59, v58
	v_fma_f32 v55, s15, v50, v48
	v_fma_f32 v58, -s15, v58, v59
	s_mov_b64 s[10:11], 0
	v_mul_f32_dpp v48, v54, v70 row_ror:8 row_mask:0xf bank_mask:0xf
	v_mul_f32_dpp v49, v53, v70 row_ror:8 row_mask:0xf bank_mask:0xf
	v_mul_f32_dpp v50, v52, v70 row_ror:8 row_mask:0xf bank_mask:0xf
	v_mul_f32_dpp v51, v55, v70 row_ror:8 row_mask:0xf bank_mask:0xf
	v_fmac_f32_dpp v54, v3, v70 row_ror:8 row_mask:0xf bank_mask:0xf
	v_fmac_f32_dpp v53, v57, v70 row_ror:8 row_mask:0xf bank_mask:0xf
	v_fmac_f32_dpp v52, v56, v70 row_ror:8 row_mask:0xf bank_mask:0xf
	v_fmac_f32_dpp v55, v58, v70 row_ror:8 row_mask:0xf bank_mask:0xf
	v_sub_f32 v3, v3, v48
	v_sub_f32 v57, v57, v49
	v_sub_f32 v56, v56, v50
	v_sub_f32 v58, v58, v51
	s_mov_b32 s18, 1
	v_readlane_b32 s24, v45, s28
	v_mov_b32_dpp v48, v54 row_half_mirror row_mask:0xf bank_mask:0xf bound_ctrl:1
	v_mov_b32_dpp v49, v53 row_half_mirror row_mask:0xf bank_mask:0xf bound_ctrl:1
	v_mov_b32_dpp v50, v52 row_half_mirror row_mask:0xf bank_mask:0xf bound_ctrl:1
	v_mov_b32_dpp v51, v55 row_half_mirror row_mask:0xf bank_mask:0xf bound_ctrl:1
	v_mov_b32_dpp v59, v3 row_half_mirror row_mask:0xf bank_mask:0xf bound_ctrl:1
	v_mov_b32_dpp v60, v57 row_half_mirror row_mask:0xf bank_mask:0xf bound_ctrl:1
	v_mov_b32_dpp v61, v56 row_half_mirror row_mask:0xf bank_mask:0xf bound_ctrl:1
	v_mov_b32_dpp v62, v58 row_half_mirror row_mask:0xf bank_mask:0xf bound_ctrl:1
	v_mul_f32_dpp v63, v48, v88 quad_perm:[3,2,1,0] row_mask:0xf bank_mask:0xf
	v_mul_f32_dpp v64, v49, v88 quad_perm:[3,2,1,0] row_mask:0xf bank_mask:0xf
	v_mul_f32_dpp v65, v50, v88 quad_perm:[3,2,1,0] row_mask:0xf bank_mask:0xf
	v_mul_f32_dpp v66, v51, v88 quad_perm:[3,2,1,0] row_mask:0xf bank_mask:0xf
	v_fmac_f32_dpp v54, v59, v88 quad_perm:[3,2,1,0] row_mask:0xf bank_mask:0xf
	v_fmac_f32_dpp v53, v60, v88 quad_perm:[3,2,1,0] row_mask:0xf bank_mask:0xf
	v_fmac_f32_dpp v52, v61, v88 quad_perm:[3,2,1,0] row_mask:0xf bank_mask:0xf
	v_fmac_f32_dpp v55, v62, v88 quad_perm:[3,2,1,0] row_mask:0xf bank_mask:0xf
	v_sub_f32 v3, v3, v63
	v_sub_f32 v57, v57, v64
	v_sub_f32 v56, v56, v65
	v_sub_f32 v58, v58, v66
	v_mov_b32_e32 v89, s23
	v_mul_f32_dpp v48, v54, v89 quad_perm:[2,3,0,1] row_mask:0xf bank_mask:0xf
	v_mul_f32_dpp v49, v53, v89 quad_perm:[2,3,0,1] row_mask:0xf bank_mask:0xf
	v_mul_f32_dpp v50, v52, v89 quad_perm:[2,3,0,1] row_mask:0xf bank_mask:0xf
	v_mul_f32_dpp v51, v55, v89 quad_perm:[2,3,0,1] row_mask:0xf bank_mask:0xf
	v_fmac_f32_dpp v54, v3, v89 quad_perm:[2,3,0,1] row_mask:0xf bank_mask:0xf
	v_fmac_f32_dpp v53, v57, v89 quad_perm:[2,3,0,1] row_mask:0xf bank_mask:0xf
	v_fmac_f32_dpp v52, v56, v89 quad_perm:[2,3,0,1] row_mask:0xf bank_mask:0xf
	v_fmac_f32_dpp v55, v58, v89 quad_perm:[2,3,0,1] row_mask:0xf bank_mask:0xf
	v_sub_f32 v3, v3, v48
	v_sub_f32 v57, v57, v49
	v_sub_f32 v56, v56, v50
	v_sub_f32 v58, v58, v51
	v_mov_b32_e32 v90, s24
	v_mul_f32_dpp v48, v54, v90 quad_perm:[1,0,3,2] row_mask:0xf bank_mask:0xf
	v_mul_f32_dpp v49, v53, v90 quad_perm:[1,0,3,2] row_mask:0xf bank_mask:0xf
	v_mul_f32_dpp v50, v52, v90 quad_perm:[1,0,3,2] row_mask:0xf bank_mask:0xf
	v_mul_f32_dpp v51, v55, v90 quad_perm:[1,0,3,2] row_mask:0xf bank_mask:0xf
	v_fmac_f32_dpp v54, v3, v90 quad_perm:[1,0,3,2] row_mask:0xf bank_mask:0xf
	v_fmac_f32_dpp v53, v57, v90 quad_perm:[1,0,3,2] row_mask:0xf bank_mask:0xf
	v_fmac_f32_dpp v52, v56, v90 quad_perm:[1,0,3,2] row_mask:0xf bank_mask:0xf
	v_fmac_f32_dpp v55, v58, v90 quad_perm:[1,0,3,2] row_mask:0xf bank_mask:0xf
	v_sub_f32 v3, v3, v48
	v_sub_f32 v57, v57, v49
	v_sub_f32 v56, v56, v50
	v_sub_f32 v58, v58, v51
	s_cbranch_vccnz .LBB0_17
	s_mov_b64 s[10:11], -1
	s_and_b64 vcc, exec, s[8:9]
	v_mul_f32_e32 v2, v46, v47
	v_mul_f32 v51, v54, v2
	v_mul_f32 v50, v3, v2
	v_mul_f32 v49, v53, v2
	v_mul_f32 v48, v57, v2
	v_mul_f32 v47, v52, v2
	v_mul_f32 v46, v56, v2
	v_mul_f32 v45, v55, v2
	v_mul_f32 v5, v58, v2
	s_cbranch_vccz .LBB0_11
	v_mov_b32_e32 v53, 1.0
	v_mov_b32_e32 v55, 0
	v_mov_b32_e32 v4, 0
	v_mov_b32_e32 v52, 0
	v_mov_b32_e32 v2, 0
	v_mov_b32_e32 v3, 0
	s_and_saveexec_b64 s[8:9], s[0:1]
	s_cbranch_execz .LBB0_23
	ds_read_b32 v4, v28 offset:264
	ds_read2_b32 v[2:3], v28 offset0:64 offset1:65
	v_mov_b32_e32 v52, 0
	v_mov_b32_e32 v53, 1.0
	s_waitcnt lgkmcnt(1)
	v_cndmask_b32_e64 v4, v4, -v4, s[2:3]
	s_waitcnt lgkmcnt(0)
	v_add_f32_e32 v3, v3, v4
	v_mul_f32_e32 v3, 0.15915494, v3
	v_cos_f32_e32 v4, v3
	v_sin_f32_e32 v54, v3
	v_cmp_gt_f32_e32 vcc, 0, v4
	s_nop 1
	v_cndmask_b32_e32 v3, v43, v44, vcc
	v_cmp_lt_f32_e64 vcc, |v4|, s16
	s_nop 1
	v_cndmask_b32_e32 v4, v4, v3, vcc
	v_div_scale_f32 v3, s[10:11], v4, v4, v54
	v_rcp_f32_e32 v56, v3
	v_div_scale_f32 v57, vcc, v54, v4, v54
	v_fma_f32 v58, -v3, v56, 1.0
	v_fmac_f32_e32 v56, v58, v56
	v_mul_f32_e32 v58, v57, v56
	v_fma_f32 v59, -v3, v58, v57
	v_fmac_f32_e32 v58, v59, v56
	v_fma_f32 v3, -v3, v58, v57
	v_div_fmas_f32 v56, v3, v56, v58
	s_and_saveexec_b64 s[10:11], s[6:7]
	s_cbranch_execz .LBB0_22
	ds_read_b32 v3, v29 offset:352
	s_waitcnt lgkmcnt(0)
	v_mul_f32_e32 v3, 0.5, v3
	v_mul_f32_e32 v3, 0.15915494, v3
	v_cos_f32_e32 v52, v3
	v_sin_f32_e32 v3, v3
	v_cmp_gt_f32_e32 vcc, 0, v52
	s_nop 1
	v_cndmask_b32_e32 v53, v43, v44, vcc
	v_cmp_lt_f32_e64 vcc, |v52|, s16
	s_nop 1
	v_cndmask_b32_e32 v53, v52, v53, vcc
	v_div_scale_f32 v52, s[14:15], v53, v53, v3
	v_rcp_f32_e32 v57, v52
	v_div_scale_f32 v58, vcc, v3, v53, v3
	v_fma_f32 v59, -v52, v57, 1.0
	v_fmac_f32_e32 v57, v59, v57
	v_mul_f32_e32 v59, v58, v57
	v_fma_f32 v60, -v52, v59, v58
	v_fmac_f32_e32 v59, v60, v57
	v_fma_f32 v52, -v52, v59, v58
	v_div_fmas_f32 v52, v52, v57, v59
	v_div_fixup_f32 v52, v52, v53, v3

.LBB0_24:
	s_lshl_b32 s10, s14, 4
	s_lshl_b32 s11, s14, 6
	v_cndmask_b32_e64 v71, 0, 1, s[8:9]
	s_or_b32 s20, s10, 1
	v_or_b32_e32 v73, s11, v36
	v_cmp_ne_u32_e32 vcc, 1, v71
	v_readlane_b32 s28, v4, s10
	v_or_b32_e32 v71, s11, v21
	v_or_b32_e32 v74, s11, v37
	v_readlane_b32 s31, v4, s20
	ds_bpermute_b32 v84, v73, v2
	v_bitop3_b32 v72, s11, 12, v21 bitop3:0x36
	v_or_b32_e32 v75, s11, v38
	v_or_b32_e32 v76, s11, v39
	ds_bpermute_b32 v78, v71, v2 offset:8
	ds_bpermute_b32 v79, v71, v3 offset:8
	ds_bpermute_b32 v80, v71, v4 offset:8
	ds_bpermute_b32 v85, v73, v3
	ds_bpermute_b32 v87, v74, v2
	ds_bpermute_b32 v88, v74, v3
	v_mov_b32_e32 v71, s28
	v_fma_f32 v98, v71, v67, v70
	v_fma_f32 v99, -v71, v68, v69
	v_fma_f32 v100, v71, v65, v64
	v_fma_f32 v101, -v71, v66, v55
	v_mov_b32_e32 v102, s31
	v_fma_f32 v68, v71, v69, v68
	v_fma_f32 v67, -v71, v70, v67
	v_fma_f32 v55, v71, v55, v66
	v_fma_f32 v64, -v71, v64, v65
	v_fma_f32 v107, v102, v60, v63
	v_fma_f32 v109, v102, v56, v59
	v_fma_f32 v110, -v102, v57, v58
	v_fma_f32 v60, -v102, v63, v60
	v_fma_f32 v57, v102, v58, v57
	v_fma_f32 v56, -v102, v59, v56
	ds_bpermute_b32 v58, v19, v67
	ds_bpermute_b32 v59, v19, v68
	ds_bpermute_b32 v63, v19, v55
	s_waitcnt lgkmcnt(4)
	v_mul_f32 v122, v84, v87
	s_waitcnt lgkmcnt(3)
	v_mul_f32 v84, v84, v88
	s_or_b32 s21, s10, 8
	s_or_b32 s15, s10, 9
	v_readlane_b32 s27, v3, s10
	v_or_b32_e32 v77, s11, v40
	ds_bpermute_b32 v81, v72, v2
	ds_bpermute_b32 v83, v72, v4
	ds_bpermute_b32 v92, v75, v2
	ds_bpermute_b32 v93, v75, v3
	ds_bpermute_b32 v94, v76, v2
	ds_bpermute_b32 v95, v76, v3
	v_fma_f32 v108, -v102, v61, v62
	v_fma_f32 v61, v102, v62, v61
	ds_bpermute_b32 v62, v19, v64
	s_waitcnt lgkmcnt(2)
	v_mul_f32 v123, v92, v94
	v_fma_f32 v88, -v85, v88, v122
	v_fma_f32 v84, v85, v87, v84
	v_fma_f32 v63, -v83, v63, v67
	v_fma_f32 v55, v80, v58, v55
	v_fma_f32 v58, -v80, v59, v64
	s_waitcnt lgkmcnt(1)
	v_fma_f32 v85, -v93, v95, v123
	v_mul_f32 v59, v88, v78
	v_mul_f32 v64, v88, v79
	v_mul_f32 v67, v88, v81
	v_readlane_b32 s19, v2, s10
	v_readlane_b32 s29, v2, s20
	v_readlane_b32 s30, v3, s20
	ds_bpermute_b32 v82, v72, v3
	v_mov_b32_e32 v91, s27
	v_readlane_b32 s27, v2, s21
	v_readlane_b32 s28, v2, s15
	v_readlane_b32 s33, v3, s21
	v_readlane_b32 s34, v3, s15
	ds_bpermute_b32 v96, v77, v2
	ds_bpermute_b32 v97, v77, v3
	ds_bpermute_b32 v112, v19, v101
	ds_bpermute_b32 v113, v19, v100
	ds_bpermute_b32 v114, v19, v60
	ds_bpermute_b32 v115, v19, v61
	ds_bpermute_b32 v116, v19, v56
	ds_bpermute_b32 v117, v19, v57
	ds_bpermute_b32 v118, v19, v108
	ds_bpermute_b32 v119, v19, v107
	ds_bpermute_b32 v120, v19, v110
	v_mul_f32 v92, v92, v95
	s_waitcnt lgkmcnt(12)
	v_fma_f32 v62, v83, v62, v68
	s_waitcnt lgkmcnt(11)
	v_mul_f32 v68, v88, v82
	s_waitcnt lgkmcnt(10)
	v_mul_f32 v88, v85, v96
	s_waitcnt lgkmcnt(9)
	v_mul_f32 v85, v85, v97
	v_fma_f32 v59, -v84, v79, v59
	v_fma_f32 v87, v93, v94, v92
	v_fma_f32 v64, v84, v78, v64
	v_fma_f32 v67, -v84, v82, v67
	ds_bpermute_b32 v86, v73, v4
	v_fma_f32 v78, -v87, v97, v88
	v_mov_b32_e32 v90, s19
	v_mov_b32_e32 v65, s29
	v_mov_b32_e32 v66, s30
	v_mov_b32_e32 v103, s27
	v_mov_b32_e32 v104, s33
	v_mov_b32_e32 v105, s28
	v_mov_b32_e32 v106, s34
	ds_bpermute_b32 v102, v19, v99
	ds_bpermute_b32 v111, v19, v98
	ds_bpermute_b32 v121, v19, v109
	s_waitcnt lgkmcnt(12)
	v_fma_f32 v92, v83, v112, v98
	s_waitcnt lgkmcnt(11)
	v_fma_f32 v93, -v83, v113, v99
	s_waitcnt lgkmcnt(2)
	v_fma_f32 v94, v80, v102, v100
	s_waitcnt lgkmcnt(1)
	v_fma_f32 v95, -v80, v111, v101
	v_fma_f32 v98, v83, v120, v107
	s_waitcnt lgkmcnt(0)
	v_fma_f32 v99, -v83, v121, v108
	v_fma_f32 v100, v80, v118, v109
	v_fma_f32 v101, -v80, v119, v110
	v_fma_f32 v61, v83, v116, v61
	v_fma_f32 v60, -v83, v117, v60
	v_fma_f32 v57, v80, v114, v57
	v_fma_f32 v56, -v80, v115, v56
	ds_swizzle_b32 v80, v58 offset:swizzle(BITMASK_PERM,"iippp")
	ds_swizzle_b32 v83, v55 offset:swizzle(BITMASK_PERM,"iippp")
	v_fma_f32 v68, v84, v81, v68
	v_fma_f32 v79, v87, v96, v85
	ds_swizzle_b32 v81, v56 offset:swizzle(BITMASK_PERM,"iippp")
	ds_swizzle_b32 v82, v57 offset:swizzle(BITMASK_PERM,"iippp")
	ds_swizzle_b32 v84, v60 offset:swizzle(BITMASK_PERM,"iippp")
	ds_swizzle_b32 v85, v61 offset:swizzle(BITMASK_PERM,"iippp")
	ds_swizzle_b32 v87, v101 offset:swizzle(BITMASK_PERM,"iippp")
	ds_swizzle_b32 v88, v100 offset:swizzle(BITMASK_PERM,"iippp")
	v_mul_f32 v112, v59, v90
	v_mul_f32 v113, v59, v91
	v_mul_f32 v114, v59, v65
	v_mul_f32 v59, v59, v66
	v_mul_f32 v115, v67, v90
	v_mul_f32 v116, v67, v91
	v_mul_f32 v117, v67, v65
	v_mul_f32 v67, v67, v66
	v_mul_f32 v118, v78, v103
	v_mul_f32 v119, v78, v104
	v_mul_f32 v120, v78, v105
	v_mul_f32 v78, v78, v106
	ds_swizzle_b32 v102, v63 offset:swizzle(BITMASK_PERM,"iippp")
	ds_swizzle_b32 v107, v62 offset:swizzle(BITMASK_PERM,"iippp")
	ds_swizzle_b32 v108, v95 offset:swizzle(BITMASK_PERM,"iippp")
	ds_swizzle_b32 v109, v94 offset:swizzle(BITMASK_PERM,"iippp")
	ds_swizzle_b32 v110, v93 offset:swizzle(BITMASK_PERM,"iippp")
	ds_swizzle_b32 v111, v92 offset:swizzle(BITMASK_PERM,"iippp")
	ds_swizzle_b32 v96, v99 offset:swizzle(BITMASK_PERM,"iippp")
	ds_swizzle_b32 v97, v98 offset:swizzle(BITMASK_PERM,"iippp")
	v_fma_f32 v112, -v64, v91, v112
	v_fma_f32 v113, v64, v90, v113
	v_fma_f32 v114, -v64, v66, v114
	v_fma_f32 v59, v64, v65, v59
	v_fma_f32 v64, -v68, v91, v115
	v_fma_f32 v90, v68, v90, v116
	v_fma_f32 v66, -v68, v66, v117
	v_fma_f32 v65, v68, v65, v67
	v_fma_f32 v67, -v79, v104, v118
	v_fma_f32 v68, v79, v103, v119
	v_fma_f32 v91, -v79, v106, v120
	v_fma_f32 v78, v79, v105, v78
	s_waitcnt lgkmcnt(3)
	v_fma_f32 v79, v86, v110, v92
	s_waitcnt lgkmcnt(2)
	v_fma_f32 v92, -v86, v111, v93
	v_fma_f32 v93, v86, v108, v94
	v_fma_f32 v94, -v86, v109, v95
	v_fma_f32 v62, v86, v102, v62
	v_fma_f32 v63, -v86, v107, v63
	v_fma_f32 v55, v86, v80, v55
	v_fma_f32 v58, -v86, v83, v58
	s_waitcnt lgkmcnt(1)
	v_fma_f32 v80, v86, v96, v98
	s_waitcnt lgkmcnt(0)
	v_fma_f32 v83, -v86, v97, v99
	v_fma_f32 v87, v86, v87, v100
	v_fma_f32 v88, -v86, v88, v101
	v_fma_f32 v61, v86, v84, v61
	v_fma_f32 v60, -v86, v85, v60
	v_fma_f32 v57, v86, v81, v57
	v_fma_f32 v56, -v86, v82, v56
	v_mov_b32_dpp v81, v58 row_half_mirror row_mask:0xf bank_mask:0xf bound_ctrl:1
	v_mov_b32_dpp v82, v55 row_half_mirror row_mask:0xf bank_mask:0xf bound_ctrl:1
	v_mov_b32_dpp v84, v63 row_half_mirror row_mask:0xf bank_mask:0xf bound_ctrl:1
	v_mov_b32_dpp v85, v62 row_half_mirror row_mask:0xf bank_mask:0xf bound_ctrl:1
	v_mov_b32_dpp v86, v94 row_half_mirror row_mask:0xf bank_mask:0xf bound_ctrl:1
	v_mov_b32_dpp v95, v93 row_half_mirror row_mask:0xf bank_mask:0xf bound_ctrl:1
	v_mov_b32_dpp v81, v81 quad_perm:[1,0,3,2] row_mask:0xf bank_mask:0xf bound_ctrl:1
	v_mov_b32_dpp v82, v82 quad_perm:[1,0,3,2] row_mask:0xf bank_mask:0xf bound_ctrl:1
	v_mov_b32_dpp v84, v84 quad_perm:[1,0,3,2] row_mask:0xf bank_mask:0xf bound_ctrl:1
	v_mov_b32_dpp v85, v85 quad_perm:[1,0,3,2] row_mask:0xf bank_mask:0xf bound_ctrl:1
	v_mov_b32_dpp v86, v86 quad_perm:[1,0,3,2] row_mask:0xf bank_mask:0xf bound_ctrl:1
	v_mov_b32_dpp v95, v95 quad_perm:[1,0,3,2] row_mask:0xf bank_mask:0xf bound_ctrl:1
	ds_bpermute_b32 v89, v74, v4
	v_readlane_b32 s35, v4, s21
	v_readlane_b32 s36, v4, s15
	v_mov_b32_dpp v96, v92 row_half_mirror row_mask:0xf bank_mask:0xf bound_ctrl:1
	v_mov_b32_dpp v97, v79 row_half_mirror row_mask:0xf bank_mask:0xf bound_ctrl:1
	v_mov_b32_dpp v98, v56 row_half_mirror row_mask:0xf bank_mask:0xf bound_ctrl:1
	v_mov_b32_dpp v99, v57 row_half_mirror row_mask:0xf bank_mask:0xf bound_ctrl:1
	v_mov_b32_dpp v100, v60 row_half_mirror row_mask:0xf bank_mask:0xf bound_ctrl:1
	v_mov_b32_dpp v101, v61 row_half_mirror row_mask:0xf bank_mask:0xf bound_ctrl:1
	v_mov_b32_dpp v102, v88 row_half_mirror row_mask:0xf bank_mask:0xf bound_ctrl:1
	v_mov_b32_dpp v103, v87 row_half_mirror row_mask:0xf bank_mask:0xf bound_ctrl:1
	v_mov_b32_dpp v104, v83 row_half_mirror row_mask:0xf bank_mask:0xf bound_ctrl:1
	v_mov_b32_dpp v105, v80 row_half_mirror row_mask:0xf bank_mask:0xf bound_ctrl:1
	v_mov_b32_dpp v96, v96 quad_perm:[1,0,3,2] row_mask:0xf bank_mask:0xf bound_ctrl:1
	v_mov_b32_dpp v97, v97 quad_perm:[1,0,3,2] row_mask:0xf bank_mask:0xf bound_ctrl:1
	v_mov_b32_dpp v98, v98 quad_perm:[1,0,3,2] row_mask:0xf bank_mask:0xf bound_ctrl:1
	v_mov_b32_dpp v99, v99 quad_perm:[1,0,3,2] row_mask:0xf bank_mask:0xf bound_ctrl:1
	v_mov_b32_dpp v100, v100 quad_perm:[1,0,3,2] row_mask:0xf bank_mask:0xf bound_ctrl:1
	v_mov_b32_dpp v101, v101 quad_perm:[1,0,3,2] row_mask:0xf bank_mask:0xf bound_ctrl:1
	v_mov_b32_dpp v102, v102 quad_perm:[1,0,3,2] row_mask:0xf bank_mask:0xf bound_ctrl:1
	v_mov_b32_dpp v103, v103 quad_perm:[1,0,3,2] row_mask:0xf bank_mask:0xf bound_ctrl:1
	v_mov_b32_dpp v104, v104 quad_perm:[1,0,3,2] row_mask:0xf bank_mask:0xf bound_ctrl:1
	v_mov_b32_dpp v105, v105 quad_perm:[1,0,3,2] row_mask:0xf bank_mask:0xf bound_ctrl:1
	s_waitcnt lgkmcnt(0)
	v_fma_f32 v79, v89, v96, v79
	s_waitcnt lgkmcnt(0)
	v_fma_f32 v92, -v89, v97, v92
	v_fma_f32 v86, v89, v86, v93
	v_fma_f32 v93, -v89, v95, v94
	v_fma_f32 v62, v89, v84, v62
	v_fma_f32 v63, -v89, v85, v63
	v_fma_f32 v55, v89, v81, v55
	v_fma_f32 v58, -v89, v82, v58
	s_waitcnt lgkmcnt(0)
	v_fma_f32 v80, v89, v104, v80
	s_waitcnt lgkmcnt(0)
	v_fma_f32 v81, -v89, v105, v83
	v_fma_f32 v82, v89, v102, v87
	v_fma_f32 v83, -v89, v103, v88
	v_fma_f32 v61, v89, v100, v61
	v_fma_f32 v60, -v89, v101, v60
	v_fma_f32 v57, v89, v98, v57
	v_fma_f32 v56, -v89, v99, v56
	v_mul_f32 v84, v112, v58
	v_mul_f32 v85, v112, v55
	v_mul_f32 v87, v64, v63
	v_mul_f32 v88, v64, v62
	v_mul_f32 v95, v64, v92
	v_mul_f32 v64, v64, v79
	v_mov_b32_e32 v69, s35
	v_mov_b32_e32 v70, s36
	v_mul_f32 v89, v112, v93
	v_mul_f32 v94, v112, v86
	v_fma_f32 v55, -v113, v55, v84
	v_fma_f32 v58, v113, v58, v85
	v_fma_f32 v62, -v90, v62, v87
	v_fma_f32 v63, v90, v63, v88
	v_mul_f32 v84, v114, v56
	v_mul_f32 v85, v114, v57
	v_mul_f32 v87, v66, v60
	v_mul_f32 v88, v66, v61
	v_mul_f32 v96, v114, v83
	v_mul_f32 v97, v114, v82
	v_mul_f32 v98, v66, v81
	v_mul_f32 v66, v66, v80
	v_fma_f32 v86, -v113, v86, v89
	v_fma_f32 v79, -v90, v79, v95
	v_fma_f32 v64, v90, v92, v64
	v_fma_f32 v57, -v59, v57, v84
	v_fma_f32 v56, v59, v56, v85
	v_fma_f32 v61, -v65, v61, v87
	v_fma_f32 v60, v65, v60, v88
	v_fma_f32 v82, -v59, v82, v96
	v_fma_f32 v59, v59, v83, v97
	v_fma_f32 v80, -v65, v80, v98
	v_fma_f32 v65, v65, v81, v66
	ds_bpermute_b32 v75, v75, v4
	v_fma_f32 v89, v113, v93, v94
	v_fma_f32 v66, v69, v82, v64
	v_fma_f32 v81, -v69, v59, v79
	v_fma_f32 v84, -v70, v65, v86
	v_fma_f32 v65, v70, v86, v65
	v_fma_f32 v59, v69, v79, v59
	v_fma_f32 v83, v70, v80, v89
	v_fma_f32 v80, -v70, v89, v80
	v_fma_f32 v64, -v69, v64, v82
	v_fma_f32 v79, v69, v55, v60
	v_fma_f32 v82, -v69, v58, v61
	v_fma_f32 v85, v70, v62, v56
	v_fma_f32 v86, -v70, v63, v57
	v_fma_f32 v57, v70, v57, v63
	v_fma_f32 v56, -v70, v56, v62
	v_fma_f32 v58, v69, v61, v58
	v_fma_f32 v55, -v69, v60, v55
	ds_bpermute_b32 v60, v20, v55
	ds_bpermute_b32 v61, v20, v58
	ds_bpermute_b32 v62, v20, v56
	ds_bpermute_b32 v63, v20, v57
	ds_bpermute_b32 v69, v20, v86
	ds_bpermute_b32 v70, v20, v85
	ds_bpermute_b32 v87, v20, v82
	ds_bpermute_b32 v92, v20, v80
	ds_bpermute_b32 v88, v20, v79
	ds_bpermute_b32 v89, v20, v64
	ds_bpermute_b32 v90, v20, v59
	ds_bpermute_b32 v93, v20, v81
	ds_bpermute_b32 v94, v20, v66
	ds_bpermute_b32 v95, v20, v84
	ds_bpermute_b32 v96, v20, v83
	ds_bpermute_b32 v97, v20, v65
	s_waitcnt lgkmcnt(4)
	v_fma_f32 v66, v75, v93, v66
	s_waitcnt lgkmcnt(3)
	v_fma_f32 v81, -v75, v94, v81
	s_waitcnt lgkmcnt(2)
	v_fma_f32 v83, v75, v95, v83
	s_waitcnt lgkmcnt(1)
	v_fma_f32 v84, -v75, v96, v84
	v_fma_f32 v65, v75, v92, v65
	s_waitcnt lgkmcnt(0)
	v_fma_f32 v80, -v75, v97, v80
	v_fma_f32 v59, v75, v89, v59
	v_fma_f32 v64, -v75, v90, v64
	v_fma_f32 v79, v75, v87, v79
	v_fma_f32 v82, -v75, v88, v82
	v_fma_f32 v69, v75, v69, v85
	v_fma_f32 v70, -v75, v70, v86
	v_fma_f32 v57, v75, v62, v57
	v_fma_f32 v56, -v75, v63, v56
	v_fma_f32 v58, v75, v60, v58
	v_fma_f32 v55, -v75, v61, v55
	s_nop 1
	v_mov_b32_dpp v60, v55 row_mirror row_mask:0xf bank_mask:0xf bound_ctrl:1
	v_mov_b32_dpp v61, v58 row_mirror row_mask:0xf bank_mask:0xf bound_ctrl:1
	v_mov_b32_dpp v62, v56 row_mirror row_mask:0xf bank_mask:0xf bound_ctrl:1
	v_mov_b32_dpp v63, v57 row_mirror row_mask:0xf bank_mask:0xf bound_ctrl:1
	v_mov_b32_dpp v75, v70 row_mirror row_mask:0xf bank_mask:0xf bound_ctrl:1
	v_mov_b32_dpp v85, v69 row_mirror row_mask:0xf bank_mask:0xf bound_ctrl:1
	v_mov_b32_dpp v86, v82 row_mirror row_mask:0xf bank_mask:0xf bound_ctrl:1
	v_mov_b32_dpp v87, v79 row_mirror row_mask:0xf bank_mask:0xf bound_ctrl:1
	v_mov_b32_dpp v92, v81 row_mirror row_mask:0xf bank_mask:0xf bound_ctrl:1
	v_mov_b32_dpp v60, v60 quad_perm:[3,2,1,0] row_mask:0xf bank_mask:0xf bound_ctrl:1
	v_mov_b32_dpp v61, v61 quad_perm:[3,2,1,0] row_mask:0xf bank_mask:0xf bound_ctrl:1
	v_mov_b32_dpp v62, v62 quad_perm:[3,2,1,0] row_mask:0xf bank_mask:0xf bound_ctrl:1
	v_mov_b32_dpp v63, v63 quad_perm:[3,2,1,0] row_mask:0xf bank_mask:0xf bound_ctrl:1
	v_mov_b32_dpp v75, v75 quad_perm:[3,2,1,0] row_mask:0xf bank_mask:0xf bound_ctrl:1
	v_mov_b32_dpp v85, v85 quad_perm:[3,2,1,0] row_mask:0xf bank_mask:0xf bound_ctrl:1
	v_mov_b32_dpp v86, v86 quad_perm:[3,2,1,0] row_mask:0xf bank_mask:0xf bound_ctrl:1
	v_mov_b32_dpp v87, v87 quad_perm:[3,2,1,0] row_mask:0xf bank_mask:0xf bound_ctrl:1
	v_mov_b32_dpp v92, v92 quad_perm:[3,2,1,0] row_mask:0xf bank_mask:0xf bound_ctrl:1
	ds_bpermute_b32 v76, v76, v4
	v_mov_b32_dpp v88, v64 row_mirror row_mask:0xf bank_mask:0xf bound_ctrl:1
	v_mov_b32_dpp v89, v59 row_mirror row_mask:0xf bank_mask:0xf bound_ctrl:1
	v_mov_b32_dpp v90, v80 row_mirror row_mask:0xf bank_mask:0xf bound_ctrl:1
	v_mov_b32_dpp v93, v66 row_mirror row_mask:0xf bank_mask:0xf bound_ctrl:1
	v_mov_b32_dpp v94, v84 row_mirror row_mask:0xf bank_mask:0xf bound_ctrl:1
	v_mov_b32_dpp v95, v83 row_mirror row_mask:0xf bank_mask:0xf bound_ctrl:1
	v_mov_b32_dpp v88, v88 quad_perm:[3,2,1,0] row_mask:0xf bank_mask:0xf bound_ctrl:1
	v_mov_b32_dpp v89, v89 quad_perm:[3,2,1,0] row_mask:0xf bank_mask:0xf bound_ctrl:1
	v_mov_b32_dpp v90, v90 quad_perm:[3,2,1,0] row_mask:0xf bank_mask:0xf bound_ctrl:1
	v_mov_b32_dpp v93, v93 quad_perm:[3,2,1,0] row_mask:0xf bank_mask:0xf bound_ctrl:1
	v_mov_b32_dpp v94, v94 quad_perm:[3,2,1,0] row_mask:0xf bank_mask:0xf bound_ctrl:1
	v_mov_b32_dpp v95, v95 quad_perm:[3,2,1,0] row_mask:0xf bank_mask:0xf bound_ctrl:1
	ds_bpermute_b32 v77, v77, v4
	v_mov_b32_dpp v96, v65 row_mirror row_mask:0xf bank_mask:0xf bound_ctrl:1
	s_nop 1
	v_mov_b32_dpp v96, v96 quad_perm:[3,2,1,0] row_mask:0xf bank_mask:0xf bound_ctrl:1
	s_waitcnt lgkmcnt(1)
	v_fma_f32 v66, v76, v92, v66
	s_waitcnt lgkmcnt(1)
	v_fma_f32 v81, -v76, v93, v81
	s_waitcnt lgkmcnt(1)
	v_fma_f32 v83, v76, v94, v83
	s_waitcnt lgkmcnt(1)
	v_fma_f32 v84, -v76, v95, v84
	v_fma_f32 v65, v76, v90, v65
	s_waitcnt lgkmcnt(0)
	v_fma_f32 v80, -v76, v96, v80
	v_fma_f32 v59, v76, v88, v59
	v_fma_f32 v64, -v76, v89, v64
	v_fma_f32 v79, v76, v86, v79
	v_fma_f32 v82, -v76, v87, v82
	v_fma_f32 v69, v76, v75, v69
	v_fma_f32 v70, -v76, v85, v70
	v_fma_f32 v57, v76, v62, v57
	v_fma_f32 v56, -v76, v63, v56
	v_fma_f32 v58, v76, v60, v58
	v_fma_f32 v55, -v76, v61, v55
	s_nop 1
	v_mov_b32_dpp v85, v82 quad_perm:[3,2,1,0] row_mask:0xf bank_mask:0xf bound_ctrl:1
	v_mov_b32_dpp v75, v70 quad_perm:[3,2,1,0] row_mask:0xf bank_mask:0xf bound_ctrl:1
	v_mov_b32_dpp v60, v55 quad_perm:[3,2,1,0] row_mask:0xf bank_mask:0xf bound_ctrl:1
	v_mov_b32_dpp v61, v58 quad_perm:[3,2,1,0] row_mask:0xf bank_mask:0xf bound_ctrl:1
	v_mov_b32_dpp v62, v56 quad_perm:[3,2,1,0] row_mask:0xf bank_mask:0xf bound_ctrl:1
	v_mov_b32_dpp v63, v57 quad_perm:[3,2,1,0] row_mask:0xf bank_mask:0xf bound_ctrl:1
	v_mov_b32_dpp v86, v79 quad_perm:[3,2,1,0] row_mask:0xf bank_mask:0xf bound_ctrl:1
	v_mov_b32_dpp v87, v64 quad_perm:[3,2,1,0] row_mask:0xf bank_mask:0xf bound_ctrl:1
	v_mov_b32_dpp v92, v84 quad_perm:[3,2,1,0] row_mask:0xf bank_mask:0xf bound_ctrl:1
	v_mov_b32_dpp v76, v69 quad_perm:[3,2,1,0] row_mask:0xf bank_mask:0xf bound_ctrl:1
	v_mov_b32_dpp v88, v59 quad_perm:[3,2,1,0] row_mask:0xf bank_mask:0xf bound_ctrl:1
	v_mov_b32_dpp v89, v80 quad_perm:[3,2,1,0] row_mask:0xf bank_mask:0xf bound_ctrl:1
	v_mov_b32_dpp v90, v65 quad_perm:[3,2,1,0] row_mask:0xf bank_mask:0xf bound_ctrl:1
	v_mov_b32_dpp v93, v83 quad_perm:[3,2,1,0] row_mask:0xf bank_mask:0xf bound_ctrl:1
	v_mov_b32_dpp v94, v81 quad_perm:[3,2,1,0] row_mask:0xf bank_mask:0xf bound_ctrl:1
	v_mov_b32_dpp v95, v66 quad_perm:[3,2,1,0] row_mask:0xf bank_mask:0xf bound_ctrl:1
	v_fma_f32 v66, v77, v94, v66
	v_fma_f32 v81, -v77, v95, v81
	v_fma_f32 v83, v77, v92, v83
	v_fma_f32 v84, -v77, v93, v84
	v_fma_f32 v65, v77, v89, v65
	v_fma_f32 v80, -v77, v90, v80
	v_fma_f32 v59, v77, v87, v59
	v_fma_f32 v64, -v77, v88, v64
	v_fma_f32 v79, v77, v85, v79
	v_fma_f32 v82, -v77, v86, v82
	v_fma_f32 v69, v77, v75, v69
	v_fma_f32 v70, -v77, v76, v70
	v_fma_f32 v57, v77, v62, v57
	v_fma_f32 v56, -v77, v63, v56
	v_fma_f32 v58, v77, v60, v58
	v_fma_f32 v55, -v77, v61, v55
	v_mul_f32 v77, v67, v82
	v_mul_f32 v75, v91, v70
	v_mul_f32 v63, v91, v57
	v_mul_f32 v62, v91, v56
	v_mul_f32 v61, v67, v58
	v_mul_f32 v60, v67, v55
	v_mul_f32 v85, v67, v79
	v_mul_f32 v86, v67, v64
	v_mul_f32 v87, v67, v59
	v_mul_f32 v92, v67, v81
	v_mul_f32 v67, v67, v66
	v_mul_f32 v76, v91, v69
	v_mul_f32 v88, v91, v80
	v_mul_f32 v89, v91, v65
	v_mul_f32 v90, v91, v84
	v_mul_f32 v91, v91, v83
	v_fma_f32 v58, -v68, v58, v60
	v_fma_f32 v55, v68, v55, v61
	v_fma_f32 v57, -v78, v57, v62
	v_fma_f32 v56, v78, v56, v63
	v_fma_f32 v60, -v78, v69, v75
	v_fma_f32 v61, v78, v70, v76
	v_fma_f32 v62, -v68, v79, v77
	v_fma_f32 v63, v68, v82, v85
	v_fma_f32 v59, -v68, v59, v86
	v_fma_f32 v64, v68, v64, v87
	v_fma_f32 v65, -v78, v65, v88
	v_fma_f32 v69, v78, v80, v89
	v_fma_f32 v70, -v78, v83, v90
	v_fma_f32 v75, v78, v84, v91
	v_fma_f32 v66, -v68, v66, v92
	v_fma_f32 v67, v68, v81, v67
	s_nop 0
	s_nop 1
	v_fmac_f32_dpp v58, v58, v23 quad_perm:[1,0,3,2] row_mask:0xf bank_mask:0xf
	v_fmac_f32_dpp v57, v57, v23 quad_perm:[1,0,3,2] row_mask:0xf bank_mask:0xf
	v_fmac_f32_dpp v60, v60, v23 quad_perm:[1,0,3,2] row_mask:0xf bank_mask:0xf
	v_fmac_f32_dpp v62, v62, v23 quad_perm:[1,0,3,2] row_mask:0xf bank_mask:0xf
	v_fmac_f32_dpp v55, v55, v23 quad_perm:[1,0,3,2] row_mask:0xf bank_mask:0xf
	v_fmac_f32_dpp v56, v56, v23 quad_perm:[1,0,3,2] row_mask:0xf bank_mask:0xf
	v_fmac_f32_dpp v61, v61, v23 quad_perm:[1,0,3,2] row_mask:0xf bank_mask:0xf
	v_fmac_f32_dpp v63, v63, v23 quad_perm:[1,0,3,2] row_mask:0xf bank_mask:0xf

	s_or_b32 s18, s10, 4
	v_fmac_f32_dpp v59, v59, v23 quad_perm:[1,0,3,2] row_mask:0xf bank_mask:0xf
	v_fmac_f32_dpp v65, v65, v23 quad_perm:[1,0,3,2] row_mask:0xf bank_mask:0xf
	v_fmac_f32_dpp v70, v70, v23 quad_perm:[1,0,3,2] row_mask:0xf bank_mask:0xf
	v_fmac_f32_dpp v66, v66, v23 quad_perm:[1,0,3,2] row_mask:0xf bank_mask:0xf
	v_fmac_f32_dpp v64, v64, v23 quad_perm:[1,0,3,2] row_mask:0xf bank_mask:0xf
	v_fmac_f32_dpp v69, v69, v23 quad_perm:[1,0,3,2] row_mask:0xf bank_mask:0xf
	v_fmac_f32_dpp v75, v75, v23 quad_perm:[1,0,3,2] row_mask:0xf bank_mask:0xf
	v_fmac_f32_dpp v67, v67, v23 quad_perm:[1,0,3,2] row_mask:0xf bank_mask:0xf

	v_fmac_f32_dpp v58, v58, v24 quad_perm:[2,3,0,1] row_mask:0xf bank_mask:0xf
	v_fmac_f32_dpp v57, v57, v24 quad_perm:[2,3,0,1] row_mask:0xf bank_mask:0xf
	v_fmac_f32_dpp v60, v60, v24 quad_perm:[2,3,0,1] row_mask:0xf bank_mask:0xf
	v_fmac_f32_dpp v62, v62, v24 quad_perm:[2,3,0,1] row_mask:0xf bank_mask:0xf
	v_fmac_f32_dpp v55, v55, v24 quad_perm:[2,3,0,1] row_mask:0xf bank_mask:0xf
	v_fmac_f32_dpp v56, v56, v24 quad_perm:[2,3,0,1] row_mask:0xf bank_mask:0xf
	v_fmac_f32_dpp v61, v61, v24 quad_perm:[2,3,0,1] row_mask:0xf bank_mask:0xf
	v_fmac_f32_dpp v63, v63, v24 quad_perm:[2,3,0,1] row_mask:0xf bank_mask:0xf

	s_or_b32 s22, s10, 3
	v_fmac_f32_dpp v59, v59, v24 quad_perm:[2,3,0,1] row_mask:0xf bank_mask:0xf
	v_fmac_f32_dpp v65, v65, v24 quad_perm:[2,3,0,1] row_mask:0xf bank_mask:0xf
	v_fmac_f32_dpp v70, v70, v24 quad_perm:[2,3,0,1] row_mask:0xf bank_mask:0xf
	v_fmac_f32_dpp v66, v66, v24 quad_perm:[2,3,0,1] row_mask:0xf bank_mask:0xf
	v_fmac_f32_dpp v64, v64, v24 quad_perm:[2,3,0,1] row_mask:0xf bank_mask:0xf
	v_fmac_f32_dpp v69, v69, v24 quad_perm:[2,3,0,1] row_mask:0xf bank_mask:0xf
	v_fmac_f32_dpp v75, v75, v24 quad_perm:[2,3,0,1] row_mask:0xf bank_mask:0xf
	v_fmac_f32_dpp v67, v67, v24 quad_perm:[2,3,0,1] row_mask:0xf bank_mask:0xf

	v_readlane_b32 s19, v52, s18
	v_mov_b32_dpp v68, v58 row_half_mirror row_mask:0xf bank_mask:0xf bound_ctrl:1
	v_mov_b32_dpp v76, v57 row_half_mirror row_mask:0xf bank_mask:0xf bound_ctrl:1
	v_mov_b32_dpp v77, v60 row_half_mirror row_mask:0xf bank_mask:0xf bound_ctrl:1
	v_mov_b32_dpp v78, v62 row_half_mirror row_mask:0xf bank_mask:0xf bound_ctrl:1
	v_mov_b32_dpp v79, v55 row_half_mirror row_mask:0xf bank_mask:0xf bound_ctrl:1
	v_mov_b32_dpp v80, v56 row_half_mirror row_mask:0xf bank_mask:0xf bound_ctrl:1
	v_mov_b32_dpp v81, v61 row_half_mirror row_mask:0xf bank_mask:0xf bound_ctrl:1
	v_mov_b32_dpp v82, v63 row_half_mirror row_mask:0xf bank_mask:0xf bound_ctrl:1
	v_mov_b32_dpp v83, v59 row_half_mirror row_mask:0xf bank_mask:0xf bound_ctrl:1
	v_mov_b32_dpp v84, v65 row_half_mirror row_mask:0xf bank_mask:0xf bound_ctrl:1
	v_mov_b32_dpp v85, v70 row_half_mirror row_mask:0xf bank_mask:0xf bound_ctrl:1
	v_mov_b32_dpp v86, v66 row_half_mirror row_mask:0xf bank_mask:0xf bound_ctrl:1
	v_mov_b32_dpp v87, v64 row_half_mirror row_mask:0xf bank_mask:0xf bound_ctrl:1
	v_mov_b32_dpp v88, v69 row_half_mirror row_mask:0xf bank_mask:0xf bound_ctrl:1
	v_mov_b32_dpp v89, v75 row_half_mirror row_mask:0xf bank_mask:0xf bound_ctrl:1
	v_mov_b32_dpp v90, v67 row_half_mirror row_mask:0xf bank_mask:0xf bound_ctrl:1
	v_fmac_f32_dpp v58, v68, v25 quad_perm:[3,2,1,0] row_mask:0xf bank_mask:0xf
	v_fmac_f32_dpp v57, v76, v25 quad_perm:[3,2,1,0] row_mask:0xf bank_mask:0xf
	v_fmac_f32_dpp v60, v77, v25 quad_perm:[3,2,1,0] row_mask:0xf bank_mask:0xf
	v_fmac_f32_dpp v62, v78, v25 quad_perm:[3,2,1,0] row_mask:0xf bank_mask:0xf
	v_fmac_f32_dpp v55, v79, v25 quad_perm:[3,2,1,0] row_mask:0xf bank_mask:0xf
	v_fmac_f32_dpp v56, v80, v25 quad_perm:[3,2,1,0] row_mask:0xf bank_mask:0xf
	v_fmac_f32_dpp v61, v81, v25 quad_perm:[3,2,1,0] row_mask:0xf bank_mask:0xf
	v_fmac_f32_dpp v63, v82, v25 quad_perm:[3,2,1,0] row_mask:0xf bank_mask:0xf

	v_fmac_f32_dpp v59, v83, v25 quad_perm:[3,2,1,0] row_mask:0xf bank_mask:0xf
	v_fmac_f32_dpp v65, v84, v25 quad_perm:[3,2,1,0] row_mask:0xf bank_mask:0xf
	v_fmac_f32_dpp v70, v85, v25 quad_perm:[3,2,1,0] row_mask:0xf bank_mask:0xf
	v_fmac_f32_dpp v66, v86, v25 quad_perm:[3,2,1,0] row_mask:0xf bank_mask:0xf
	v_fmac_f32_dpp v64, v87, v25 quad_perm:[3,2,1,0] row_mask:0xf bank_mask:0xf
	v_fmac_f32_dpp v69, v88, v25 quad_perm:[3,2,1,0] row_mask:0xf bank_mask:0xf
	v_fmac_f32_dpp v75, v89, v25 quad_perm:[3,2,1,0] row_mask:0xf bank_mask:0xf
	v_fmac_f32_dpp v67, v90, v25 quad_perm:[3,2,1,0] row_mask:0xf bank_mask:0xf

	v_readlane_b32 s18, v52, s22
	s_nop 1
	v_fmac_f32_dpp v58, v58, v26 row_ror:8 row_mask:0xf bank_mask:0xf
	v_fmac_f32_dpp v57, v57, v26 row_ror:8 row_mask:0xf bank_mask:0xf
	v_fmac_f32_dpp v60, v60, v26 row_ror:8 row_mask:0xf bank_mask:0xf
	v_fmac_f32_dpp v62, v62, v26 row_ror:8 row_mask:0xf bank_mask:0xf
	v_fmac_f32_dpp v55, v55, v26 row_ror:8 row_mask:0xf bank_mask:0xf
	v_fmac_f32_dpp v56, v56, v26 row_ror:8 row_mask:0xf bank_mask:0xf
	v_fmac_f32_dpp v61, v61, v26 row_ror:8 row_mask:0xf bank_mask:0xf
	v_fmac_f32_dpp v63, v63, v26 row_ror:8 row_mask:0xf bank_mask:0xf

	v_fmac_f32_dpp v59, v59, v26 row_ror:8 row_mask:0xf bank_mask:0xf
	v_fmac_f32_dpp v65, v65, v26 row_ror:8 row_mask:0xf bank_mask:0xf
	v_fmac_f32_dpp v70, v70, v26 row_ror:8 row_mask:0xf bank_mask:0xf
	v_fmac_f32_dpp v66, v66, v26 row_ror:8 row_mask:0xf bank_mask:0xf
	v_fmac_f32_dpp v64, v64, v26 row_ror:8 row_mask:0xf bank_mask:0xf
	v_fmac_f32_dpp v69, v69, v26 row_ror:8 row_mask:0xf bank_mask:0xf
	v_fmac_f32_dpp v75, v75, v26 row_ror:8 row_mask:0xf bank_mask:0xf
	v_fmac_f32_dpp v67, v67, v26 row_ror:8 row_mask:0xf bank_mask:0xf

	s_or_b32 s23, s10, 2
	v_add_f32 v68, v58, v57
	v_sub_f32 v57, v58, v57
	v_add_f32 v58, v55, v56
	v_sub_f32 v55, v55, v56
	v_add_f32 v56, v60, v62
	v_sub_f32 v60, v60, v62
	v_add_f32 v62, v61, v63
	v_sub_f32 v61, v61, v63
	v_add_f32 v63, v59, v65
	v_sub_f32 v59, v59, v65
	v_add_f32 v65, v64, v69
	v_sub_f32 v64, v64, v69
	v_add_f32 v69, v70, v66
	v_sub_f32 v66, v70, v66
	v_add_f32 v70, v75, v67
	v_sub_f32 v67, v75, v67
	v_add_f32 v75, v68, v56
	v_sub_f32 v56, v68, v56
	v_add_f32 v68, v58, v62
	v_sub_f32 v58, v58, v62
	v_add_f32 v62, v57, v60
	v_sub_f32 v57, v57, v60
	v_add_f32 v60, v55, v61
	v_sub_f32 v55, v55, v61
	v_add_f32 v61, v63, v69
	v_sub_f32 v63, v63, v69
	v_add_f32 v69, v65, v70
	v_sub_f32 v65, v65, v70
	v_add_f32 v70, v59, v66
	v_sub_f32 v59, v59, v66
	v_add_f32 v66, v64, v67
	v_sub_f32 v64, v64, v67
	v_add_f32 v67, v75, v61
	v_sub_f32 v61, v75, v61
	v_add_f32 v75, v68, v69
	v_sub_f32 v68, v68, v69
	v_add_f32 v69, v62, v70
	v_sub_f32 v62, v62, v70
	v_add_f32 v70, v60, v66
	v_sub_f32 v60, v60, v66
	v_add_f32 v66, v56, v63
	v_sub_f32 v56, v56, v63
	v_add_f32 v63, v58, v65
	v_sub_f32 v58, v58, v65
	v_add_f32 v65, v57, v59
	v_sub_f32 v57, v57, v59
	v_add_f32 v59, v55, v64
	v_sub_f32 v55, v55, v64
	v_readlane_b32 s15, v52, s23
	s_nop 1
	v_permlane16_swap_b32 v67, v69
	v_permlane16_swap_b32 v75, v70
	v_permlane16_swap_b32 v66, v65
	v_permlane16_swap_b32 v63, v59
	v_permlane16_swap_b32 v61, v62
	v_permlane16_swap_b32 v68, v60
	v_permlane16_swap_b32 v56, v57
	v_permlane16_swap_b32 v58, v55
	s_or_b32 s24, s10, 5
	v_permlane32_swap_b32 v67, v66
	v_permlane32_swap_b32 v75, v63
	v_permlane32_swap_b32 v69, v65
	v_permlane32_swap_b32 v70, v59
	v_permlane32_swap_b32 v61, v56
	v_permlane32_swap_b32 v68, v58
	v_permlane32_swap_b32 v62, v57
	v_permlane32_swap_b32 v60, v55
	v_readlane_b32 s11, v52, s20
	v_add_f32 v64, v67, v69
	v_sub_f32 v67, v67, v69
	v_add_f32 v69, v75, v70
	v_sub_f32 v70, v75, v70
	v_add_f32 v75, v66, v65
	v_sub_f32 v65, v66, v65
	v_add_f32 v66, v63, v59
	v_sub_f32 v59, v63, v59
	v_add_f32 v63, v61, v62
	v_sub_f32 v61, v61, v62
	v_add_f32 v62, v68, v60
	v_sub_f32 v60, v68, v60
	v_add_f32 v68, v56, v57
	v_sub_f32 v56, v56, v57
	v_add_f32 v57, v58, v55
	v_sub_f32 v55, v58, v55
	v_add_f32 v58, v64, v75
	v_sub_f32 v64, v64, v75
	v_add_f32 v75, v69, v66
	v_sub_f32 v66, v69, v66
	v_add_f32 v69, v67, v65
	v_sub_f32 v65, v67, v65
	v_add_f32 v67, v70, v59
	v_sub_f32 v59, v70, v59
	v_add_f32 v70, v63, v68
	v_sub_f32 v63, v63, v68
	v_add_f32 v68, v62, v57
	v_sub_f32 v57, v62, v57
	v_add_f32 v62, v61, v56
	v_sub_f32 v56, v61, v56
	v_add_f32 v61, v60, v55
	v_sub_f32 v55, v60, v55
	v_mul_f32 v58, v58, v11
	v_mul_f32 v60, v75, v11
	v_mul_f32 v69, v69, v12
	v_mul_f32 v67, v67, v12
	v_mul_f32 v64, v64, v13
	v_mul_f32 v66, v66, v13
	v_mul_f32 v65, v65, v14
	v_mul_f32 v59, v59, v14
	v_mul_f32 v70, v70, v15
	v_mul_f32 v68, v68, v15
	v_mul_f32 v62, v62, v16
	v_mul_f32 v61, v61, v16
	v_mul_f32 v56, v56, v18
	v_mul_f32 v55, v55, v18
	v_mul_f32 v63, v63, v17
	v_mul_f32 v57, v57, v17
	s_nop 0
	v_fma_f32 v75, s19, v67, v58
	v_fma_f32 v76, -s19, v69, v60
	v_fma_f32 v60, s19, v60, v69
	v_fma_f32 v58, -s19, v58, v67
	v_fma_f32 v67, s19, v59, v64
	v_fma_f32 v69, -s19, v65, v66
	v_fma_f32 v65, s19, v66, v65
	v_fma_f32 v59, -s19, v64, v59
	v_fma_f32 v64, s19, v61, v70
	v_fma_f32 v66, -s19, v62, v68
	v_fma_f32 v62, s19, v68, v62
	v_fma_f32 v61, -s19, v70, v61
	v_fma_f32 v68, s19, v55, v63
	v_fma_f32 v70, -s19, v56, v57
	v_fma_f32 v56, s19, v57, v56
	v_fma_f32 v55, -s19, v63, v55
	s_nop 0
	v_fma_f32 v57, s18, v69, v75
	v_fma_f32 v63, -s18, v67, v76
	v_fma_f32 v67, s18, v76, v67
	v_fma_f32 v69, -s18, v75, v69
	v_fma_f32 v75, s18, v59, v60
	v_fma_f32 v76, -s18, v65, v58
	v_fma_f32 v58, s18, v58, v65
	v_fma_f32 v59, -s18, v60, v59
	v_fma_f32 v60, s18, v70, v64
	v_fma_f32 v65, -s18, v68, v66
	v_fma_f32 v66, s18, v66, v68
	v_fma_f32 v64, -s18, v64, v70
	v_fma_f32 v68, s18, v55, v62
	v_fma_f32 v70, -s18, v56, v61
	v_fma_f32 v56, s18, v61, v56
	v_fma_f32 v55, -s18, v62, v55
	s_nop 0
	s_nop 1
	v_permlane32_swap_b32 v57, v67
	v_permlane32_swap_b32 v63, v69
	v_permlane32_swap_b32 v75, v58
	v_permlane32_swap_b32 v76, v59
	s_or_b32 s25, s10, 6
	v_permlane32_swap_b32 v60, v66
	v_permlane32_swap_b32 v65, v64
	v_permlane32_swap_b32 v68, v56
	v_permlane32_swap_b32 v70, v55
	v_permlane16_swap_b32 v57, v75
	v_permlane16_swap_b32 v63, v76
	v_permlane16_swap_b32 v67, v58
	v_permlane16_swap_b32 v69, v59
	s_or_b32 s26, s10, 7
	v_permlane16_swap_b32 v60, v68
	v_permlane16_swap_b32 v65, v70
	v_permlane16_swap_b32 v66, v56
	v_permlane16_swap_b32 v64, v55
	v_fma_f32 v61, s15, v76, v57
	v_fma_f32 v62, -s15, v75, v63
	v_fma_f32 v63, s15, v63, v75
	v_fma_f32 v57, -s15, v57, v76
	v_fma_f32 v75, s15, v59, v67
	v_fma_f32 v76, -s15, v58, v69
	v_fma_f32 v58, s15, v69, v58
	v_fma_f32 v59, -s15, v67, v59
	s_nop 0
	v_fma_f32 v67, s15, v70, v60
	v_fma_f32 v69, -s15, v68, v65
	v_fma_f32 v60, -s15, v60, v70
	v_fma_f32 v70, -s15, v56, v64
	v_fma_f32 v65, s15, v65, v68
	v_fma_f32 v68, s15, v55, v66
	v_fma_f32 v56, s15, v64, v56
	v_fma_f32 v55, -s15, v66, v55
	v_fma_f32 v64, s11, v76, v61
	v_fma_f32 v77, -s11, v75, v62
	v_fma_f32 v75, s11, v62, v75
	v_fma_f32 v61, -s11, v61, v76
	v_fma_f32 v76, s11, v59, v63
	v_fma_f32 v62, -s11, v58, v57
	v_fma_f32 v78, s11, v57, v58
	v_fma_f32 v79, -s11, v63, v59
	s_nop 0
	v_fma_f32 v57, s11, v70, v67
	v_fma_f32 v59, -s11, v68, v69
	v_fma_f32 v69, s11, v69, v68
	v_fma_f32 v70, -s11, v67, v70
	v_fma_f32 v63, s11, v55, v65
	v_readlane_b32 s10, v52, s10
	v_readlane_b32 s20, v52, s24
	v_fma_f32 v80, -s11, v56, v60
	v_fma_f32 v81, s11, v60, v56
	v_fma_f32 v82, -s11, v65, v55
	v_fma_f32 v65, s10, v59, v64
	v_fma_f32 v66, -s10, v57, v77
	v_fma_f32 v58, s10, v77, v57
	v_fma_f32 v59, -s10, v64, v59
	s_nop 0
	v_fma_f32 v67, s10, v80, v76
	v_fma_f32 v68, -s10, v63, v62
	v_fma_f32 v62, s10, v62, v63
	v_fma_f32 v63, -s10, v76, v80
	v_fma_f32 v56, s10, v70, v75
	v_fma_f32 v57, -s10, v69, v61
	v_fma_f32 v55, s10, v61, v69
	v_fma_f32 v64, -s10, v75, v70
	v_fma_f32 v60, s10, v82, v78
	v_fma_f32 v61, -s10, v81, v79
	v_fma_f32 v69, s10, v79, v81
	v_fma_f32 v70, -s10, v78, v82
	s_nop 0
	v_mov_b32_e32 v74, s20
	s_nop 1
	v_mul_f32_dpp v75, v65, v74 row_ror:8 row_mask:0xf bank_mask:0xf
	v_mul_f32_dpp v76, v67, v74 row_ror:8 row_mask:0xf bank_mask:0xf
	v_mul_f32_dpp v77, v56, v74 row_ror:8 row_mask:0xf bank_mask:0xf
	v_mul_f32_dpp v78, v60, v74 row_ror:8 row_mask:0xf bank_mask:0xf
	v_fmac_f32_dpp v65, v66, v74 row_ror:8 row_mask:0xf bank_mask:0xf
	v_fmac_f32_dpp v67, v68, v74 row_ror:8 row_mask:0xf bank_mask:0xf
	v_fmac_f32_dpp v56, v57, v74 row_ror:8 row_mask:0xf bank_mask:0xf
	v_fmac_f32_dpp v60, v61, v74 row_ror:8 row_mask:0xf bank_mask:0xf
	v_sub_f32 v66, v66, v75
	v_sub_f32 v68, v68, v76
	v_sub_f32 v57, v57, v77
	v_sub_f32 v61, v61, v78
	v_readlane_b32 s22, v52, s25
	s_nop 1
	v_mul_f32_dpp v75, v58, v74 row_ror:8 row_mask:0xf bank_mask:0xf
	v_mul_f32_dpp v76, v62, v74 row_ror:8 row_mask:0xf bank_mask:0xf
	v_mul_f32_dpp v77, v55, v74 row_ror:8 row_mask:0xf bank_mask:0xf
	v_mul_f32_dpp v78, v69, v74 row_ror:8 row_mask:0xf bank_mask:0xf
	v_fmac_f32_dpp v58, v59, v74 row_ror:8 row_mask:0xf bank_mask:0xf
	v_fmac_f32_dpp v62, v63, v74 row_ror:8 row_mask:0xf bank_mask:0xf
	v_fmac_f32_dpp v55, v64, v74 row_ror:8 row_mask:0xf bank_mask:0xf
	v_fmac_f32_dpp v69, v70, v74 row_ror:8 row_mask:0xf bank_mask:0xf
	v_sub_f32 v59, v59, v75
	v_sub_f32 v63, v63, v76
	v_sub_f32 v64, v64, v77
	v_sub_f32 v70, v70, v78
	v_readlane_b32 s23, v52, s26
	v_mov_b32_dpp v74, v65 row_half_mirror row_mask:0xf bank_mask:0xf bound_ctrl:1
	v_mov_b32_dpp v75, v67 row_half_mirror row_mask:0xf bank_mask:0xf bound_ctrl:1
	v_mov_b32_dpp v76, v56 row_half_mirror row_mask:0xf bank_mask:0xf bound_ctrl:1
	v_mov_b32_dpp v77, v60 row_half_mirror row_mask:0xf bank_mask:0xf bound_ctrl:1
	v_mov_b32_e32 v73, s22
	v_mov_b32_dpp v78, v66 row_half_mirror row_mask:0xf bank_mask:0xf bound_ctrl:1
	v_mov_b32_dpp v79, v68 row_half_mirror row_mask:0xf bank_mask:0xf bound_ctrl:1
	v_mov_b32_dpp v80, v57 row_half_mirror row_mask:0xf bank_mask:0xf bound_ctrl:1
	v_mov_b32_dpp v81, v61 row_half_mirror row_mask:0xf bank_mask:0xf bound_ctrl:1
	v_mov_b32_dpp v82, v58 row_half_mirror row_mask:0xf bank_mask:0xf bound_ctrl:1
	v_mov_b32_dpp v83, v62 row_half_mirror row_mask:0xf bank_mask:0xf bound_ctrl:1
	v_mov_b32_dpp v84, v55 row_half_mirror row_mask:0xf bank_mask:0xf bound_ctrl:1
	v_mov_b32_dpp v85, v69 row_half_mirror row_mask:0xf bank_mask:0xf bound_ctrl:1
	v_mov_b32_dpp v86, v59 row_half_mirror row_mask:0xf bank_mask:0xf bound_ctrl:1
	v_mov_b32_dpp v87, v63 row_half_mirror row_mask:0xf bank_mask:0xf bound_ctrl:1
	v_mov_b32_dpp v88, v64 row_half_mirror row_mask:0xf bank_mask:0xf bound_ctrl:1
	v_mov_b32_dpp v89, v70 row_half_mirror row_mask:0xf bank_mask:0xf bound_ctrl:1
	v_mul_f32_dpp v90, v74, v73 quad_perm:[3,2,1,0] row_mask:0xf bank_mask:0xf
	v_mul_f32_dpp v91, v75, v73 quad_perm:[3,2,1,0] row_mask:0xf bank_mask:0xf
	v_mul_f32_dpp v92, v76, v73 quad_perm:[3,2,1,0] row_mask:0xf bank_mask:0xf
	v_mul_f32_dpp v93, v77, v73 quad_perm:[3,2,1,0] row_mask:0xf bank_mask:0xf
	v_fmac_f32_dpp v65, v78, v73 quad_perm:[3,2,1,0] row_mask:0xf bank_mask:0xf
	v_fmac_f32_dpp v67, v79, v73 quad_perm:[3,2,1,0] row_mask:0xf bank_mask:0xf
	v_fmac_f32_dpp v56, v80, v73 quad_perm:[3,2,1,0] row_mask:0xf bank_mask:0xf
	v_fmac_f32_dpp v60, v81, v73 quad_perm:[3,2,1,0] row_mask:0xf bank_mask:0xf
	v_sub_f32 v66, v66, v90
	v_sub_f32 v68, v68, v91
	v_sub_f32 v57, v57, v92
	v_sub_f32 v61, v61, v93
	v_mul_f32_dpp v74, v82, v73 quad_perm:[3,2,1,0] row_mask:0xf bank_mask:0xf
	v_mul_f32_dpp v75, v83, v73 quad_perm:[3,2,1,0] row_mask:0xf bank_mask:0xf
	v_mul_f32_dpp v76, v84, v73 quad_perm:[3,2,1,0] row_mask:0xf bank_mask:0xf
	v_mul_f32_dpp v77, v85, v73 quad_perm:[3,2,1,0] row_mask:0xf bank_mask:0xf
	v_fmac_f32_dpp v58, v86, v73 quad_perm:[3,2,1,0] row_mask:0xf bank_mask:0xf
	v_fmac_f32_dpp v62, v87, v73 quad_perm:[3,2,1,0] row_mask:0xf bank_mask:0xf
	v_fmac_f32_dpp v55, v88, v73 quad_perm:[3,2,1,0] row_mask:0xf bank_mask:0xf
	v_fmac_f32_dpp v69, v89, v73 quad_perm:[3,2,1,0] row_mask:0xf bank_mask:0xf
	v_sub_f32 v59, v59, v74
	v_sub_f32 v63, v63, v75
	v_sub_f32 v64, v64, v76
	v_sub_f32 v70, v70, v77
	s_mov_b64 s[8:9], 0
	s_mov_b32 s14, 1
	v_readlane_b32 s21, v52, s21
	s_and_b64 vcc, exec, vcc
	v_mov_b32_e32 v72, s23
	s_nop 1
	v_mul_f32_dpp v73, v65, v72 quad_perm:[2,3,0,1] row_mask:0xf bank_mask:0xf
	v_mul_f32_dpp v74, v67, v72 quad_perm:[2,3,0,1] row_mask:0xf bank_mask:0xf
	v_mul_f32_dpp v75, v56, v72 quad_perm:[2,3,0,1] row_mask:0xf bank_mask:0xf
	v_mul_f32_dpp v76, v60, v72 quad_perm:[2,3,0,1] row_mask:0xf bank_mask:0xf
	v_fmac_f32_dpp v65, v66, v72 quad_perm:[2,3,0,1] row_mask:0xf bank_mask:0xf
	v_fmac_f32_dpp v67, v68, v72 quad_perm:[2,3,0,1] row_mask:0xf bank_mask:0xf
	v_fmac_f32_dpp v56, v57, v72 quad_perm:[2,3,0,1] row_mask:0xf bank_mask:0xf
	v_fmac_f32_dpp v60, v61, v72 quad_perm:[2,3,0,1] row_mask:0xf bank_mask:0xf
	v_sub_f32 v66, v66, v73
	v_sub_f32 v68, v68, v74
	v_sub_f32 v57, v57, v75
	v_sub_f32 v61, v61, v76
	v_mov_b32_e32 v71, s21
	v_mul_f32_dpp v73, v58, v72 quad_perm:[2,3,0,1] row_mask:0xf bank_mask:0xf
	v_mul_f32_dpp v74, v62, v72 quad_perm:[2,3,0,1] row_mask:0xf bank_mask:0xf
	v_mul_f32_dpp v75, v55, v72 quad_perm:[2,3,0,1] row_mask:0xf bank_mask:0xf
	v_mul_f32_dpp v76, v69, v72 quad_perm:[2,3,0,1] row_mask:0xf bank_mask:0xf
	v_fmac_f32_dpp v58, v59, v72 quad_perm:[2,3,0,1] row_mask:0xf bank_mask:0xf
	v_fmac_f32_dpp v62, v63, v72 quad_perm:[2,3,0,1] row_mask:0xf bank_mask:0xf
	v_fmac_f32_dpp v55, v64, v72 quad_perm:[2,3,0,1] row_mask:0xf bank_mask:0xf
	v_fmac_f32_dpp v69, v70, v72 quad_perm:[2,3,0,1] row_mask:0xf bank_mask:0xf
	v_sub_f32 v59, v59, v73
	v_sub_f32 v63, v63, v74
	v_sub_f32 v64, v64, v75
	v_sub_f32 v70, v70, v76
	s_nop 0
	s_nop 1
	v_mul_f32_dpp v72, v65, v71 quad_perm:[1,0,3,2] row_mask:0xf bank_mask:0xf
	v_mul_f32_dpp v73, v67, v71 quad_perm:[1,0,3,2] row_mask:0xf bank_mask:0xf
	v_mul_f32_dpp v74, v56, v71 quad_perm:[1,0,3,2] row_mask:0xf bank_mask:0xf
	v_mul_f32_dpp v75, v60, v71 quad_perm:[1,0,3,2] row_mask:0xf bank_mask:0xf
	v_fmac_f32_dpp v65, v66, v71 quad_perm:[1,0,3,2] row_mask:0xf bank_mask:0xf
	v_fmac_f32_dpp v67, v68, v71 quad_perm:[1,0,3,2] row_mask:0xf bank_mask:0xf
	v_fmac_f32_dpp v56, v57, v71 quad_perm:[1,0,3,2] row_mask:0xf bank_mask:0xf
	v_fmac_f32_dpp v60, v61, v71 quad_perm:[1,0,3,2] row_mask:0xf bank_mask:0xf
	v_sub_f32 v66, v66, v72
	v_sub_f32 v68, v68, v73
	v_sub_f32 v57, v57, v74
	v_sub_f32 v61, v61, v75
	s_nop 0
	s_nop 1
	v_mul_f32_dpp v72, v58, v71 quad_perm:[1,0,3,2] row_mask:0xf bank_mask:0xf
	v_mul_f32_dpp v73, v62, v71 quad_perm:[1,0,3,2] row_mask:0xf bank_mask:0xf
	v_mul_f32_dpp v74, v55, v71 quad_perm:[1,0,3,2] row_mask:0xf bank_mask:0xf
	v_mul_f32_dpp v75, v69, v71 quad_perm:[1,0,3,2] row_mask:0xf bank_mask:0xf
	v_fmac_f32_dpp v58, v59, v71 quad_perm:[1,0,3,2] row_mask:0xf bank_mask:0xf
	v_fmac_f32_dpp v62, v63, v71 quad_perm:[1,0,3,2] row_mask:0xf bank_mask:0xf
	v_fmac_f32_dpp v55, v64, v71 quad_perm:[1,0,3,2] row_mask:0xf bank_mask:0xf
	v_fmac_f32_dpp v69, v70, v71 quad_perm:[1,0,3,2] row_mask:0xf bank_mask:0xf
	v_sub_f32 v59, v59, v72
	v_sub_f32 v63, v63, v73
	v_sub_f32 v64, v64, v74
	v_sub_f32 v70, v70, v75
	s_cbranch_vccz .LBB0_24
	v_mul_f32_e32 v2, v53, v54
	v_mul_f32 v3, v65, v2
	v_mul_f32 v55, v57, v2
	v_mul_f32 v4, v66, v2
	v_mul_f32 v52, v67, v2
	v_mul_f32 v53, v68, v2
	v_mul_f32 v54, v56, v2
	v_mul_f32 v57, v3, v3
	v_mul_f32 v56, v60, v2
	v_mul_f32 v2, v61, v2
	s_mov_b64 s[10:11], 0
	v_fma_f32 v57, v4, v4, v57
	s_nop 0
	v_fma_f32 v57, v52, v52, v57
	s_nop 0
	v_fma_f32 v57, v53, v53, v57
	s_nop 0
	v_fma_f32 v57, v54, v54, v57
	s_nop 0
	v_fma_f32 v57, v55, v55, v57
	s_nop 0
	v_fma_f32 v57, v56, v56, v57
	s_nop 0
	v_fma_f32 v57, v2, v2, v57
	s_nop 1
	v_add_f32_dpp v57, v57, v57 quad_perm:[1,0,3,2] row_mask:0xf bank_mask:0xf bound_ctrl:1
	s_nop 1
	v_add_f32_dpp v57, v57, v57 quad_perm:[2,3,0,1] row_mask:0xf bank_mask:0xf bound_ctrl:1
	ds_swizzle_b32 v58, v57 offset:swizzle(SWAP,4)
	s_waitcnt lgkmcnt(0)
	v_add_f32_e32 v57, v57, v58
	s_nop 1
	v_add_f32_dpp v57, v57, v57 row_ror:8 row_mask:0xf bank_mask:0xf bound_ctrl:1
	ds_swizzle_b32 v58, v57 offset:swizzle(SWAP,16)
	s_waitcnt lgkmcnt(0)
	v_add_f32_e32 v57, v57, v58
	ds_bpermute_b32 v58, v19, v57
	s_waitcnt lgkmcnt(0)
	v_add_f32_e32 v57, v57, v58
	v_mul_f32_e32 v58, 0x4f800000, v57
	v_cmp_gt_f32_e32 vcc, s17, v57
	s_nop 1
	v_cndmask_b32_e32 v57, v57, v58, vcc
	v_sqrt_f32_e32 v58, v57
	s_nop 0
	v_add_u32_e32 v59, -1, v58
	v_add_u32_e32 v60, 1, v58
	v_fma_f32 v61, -v59, v58, v57
	v_fma_f32 v62, -v60, v58, v57
	v_cmp_ge_f32_e64 s[8:9], 0, v61
	s_nop 1
	v_cndmask_b32_e64 v58, v58, v59, s[8:9]
	v_cmp_lt_f32_e64 s[8:9], 0, v62
	s_nop 1
	v_cndmask_b32_e64 v58, v58, v60, s[8:9]
	v_mul_f32_e32 v59, 0x37800000, v58
	v_cndmask_b32_e32 v58, v58, v59, vcc
	v_cmp_class_f32_e32 vcc, v57, v41
	s_nop 1
	v_cndmask_b32_e32 v57, v58, v57, vcc
	v_add_f32_e32 v57, 0x322bcc77, v57
	v_div_scale_f32 v58, s[8:9], v57, v57, 1.0
	v_rcp_f32_e32 v59, v58
	v_div_scale_f32 v60, vcc, 1.0, v57, 1.0
	v_fma_f32 v61, -v58, v59, 1.0
	v_fmac_f32_e32 v59, v61, v59
	v_mul_f32_e32 v61, v60, v59
	v_fma_f32 v62, -v58, v61, v60
	v_fmac_f32_e32 v61, v62, v59
	v_fma_f32 v58, -v58, v61, v60
	v_div_fmas_f32 v58, v58, v59, v61
	v_div_fixup_f32 v57, v58, v57, 1.0
	v_mul_f32 v3, v3, v57
	v_mul_f32 v4, v4, v57
	v_mul_f32 v52, v52, v57
	v_mul_f32 v53, v53, v57
	v_mul_f32 v2, v2, v57
	s_nop 0
	v_mul_f32 v58, v3, v42
	s_nop 0
	v_max_f32 v3, v3, v58
	v_mul_f32 v58, v4, v42
	s_nop 0
	v_max_f32 v4, v4, v58
	v_mul_f32 v58, v52, v42
	s_nop 0
	v_max_f32 v52, v52, v58
	v_mul_f32 v58, v53, v42
	s_nop 0
	v_max_f32 v58, v53, v58
	v_mul_f32 v53, v54, v57
	v_mul_f32 v54, v55, v57
	s_nop 0
	v_mul_f32 v55, v53, v42
	s_nop 0
	v_max_f32 v55, v53, v55
	v_mul_f32 v53, v54, v42
	s_nop 0
	v_max_f32 v59, v54, v53
	v_mul_f32 v53, v56, v57
	s_nop 0
	v_mul_f32 v54, v53, v42
	s_nop 0
	v_max_f32 v60, v53, v54
	v_mul_f32 v53, v2, v42
	s_nop 0
	v_max_f32 v2, v2, v53
	v_mul_f32 v53, v3, v3
	s_nop 0
	v_fma_f32 v53, v4, v4, v53
	s_nop 0
	v_fma_f32 v53, v52, v52, v53
	s_nop 0
	v_fma_f32 v53, v58, v58, v53
	s_nop 0
	v_fma_f32 v53, v55, v55, v53
	s_nop 0
	v_fma_f32 v53, v59, v59, v53
	s_nop 0
	v_fma_f32 v53, v60, v60, v53
	s_nop 0
	v_fma_f32 v53, v2, v2, v53
	s_nop 1
	v_add_f32_dpp v53, v53, v53 quad_perm:[1,0,3,2] row_mask:0xf bank_mask:0xf bound_ctrl:1
	s_nop 1
	v_add_f32_dpp v53, v53, v53 quad_perm:[2,3,0,1] row_mask:0xf bank_mask:0xf bound_ctrl:1
	ds_swizzle_b32 v54, v53 offset:swizzle(SWAP,4)
	s_waitcnt lgkmcnt(0)
	v_add_f32_e32 v53, v53, v54
	s_nop 1
	v_add_f32_dpp v53, v53, v53 row_ror:8 row_mask:0xf bank_mask:0xf bound_ctrl:1
	ds_swizzle_b32 v54, v53 offset:swizzle(SWAP,16)
	s_waitcnt lgkmcnt(0)
	v_add_f32_e32 v53, v53, v54
	ds_bpermute_b32 v54, v19, v53
	s_waitcnt lgkmcnt(0)
	v_add_f32_e32 v53, v53, v54
	v_mul_f32_e32 v54, 0x4f800000, v53
	v_cmp_gt_f32_e32 vcc, s17, v53
	s_nop 1
	v_cndmask_b32_e32 v53, v53, v54, vcc
	v_sqrt_f32_e32 v54, v53
	s_nop 0
	v_add_u32_e32 v56, -1, v54
	v_fma_f32 v57, -v56, v54, v53
	v_cmp_ge_f32_e64 s[8:9], 0, v57
	v_add_u32_e32 v57, 1, v54
	s_nop 0
	v_cndmask_b32_e64 v56, v54, v56, s[8:9]
	v_fma_f32 v54, -v57, v54, v53
	v_cmp_lt_f32_e64 s[8:9], 0, v54
	s_nop 1
	v_cndmask_b32_e64 v54, v56, v57, s[8:9]
	v_mul_f32_e32 v56, 0x37800000, v54
	v_cndmask_b32_e32 v54, v54, v56, vcc
	v_cmp_class_f32_e32 vcc, v53, v41
	s_nop 1
	v_cndmask_b32_e32 v53, v54, v53, vcc
	v_div_scale_f32 v54, s[8:9], v53, v53, 1.0
	v_rcp_f32_e32 v56, v54
	s_nop 0
	v_fma_f32 v57, -v54, v56, 1.0
	v_fmac_f32_e32 v56, v57, v56
	v_div_scale_f32 v57, vcc, 1.0, v53, 1.0
	v_mul_f32_e32 v61, v57, v56
	v_fma_f32 v62, -v54, v61, v57
	v_fmac_f32_e32 v61, v62, v56
	v_fma_f32 v54, -v54, v61, v57
	v_div_fmas_f32 v54, v54, v56, v61
	v_div_fixup_f32 v61, v54, v53, 1.0
	v_mul_f32 v54, v3, v61
	v_mul_f32 v3, v4, v61
	v_mul_f32 v53, v52, v61
	v_mul_f32 v57, v58, v61
	v_mul_f32 v52, v55, v61
	v_mul_f32 v56, v59, v61
	v_mul_f32 v55, v60, v61
	v_mul_f32 v58, v2, v61
	s_branch .LBB0_11
